# speedup vs baseline: 1.2495x; 1.1164x over previous
.LBB0_65:
	s_or_b64 exec, exec, s[12:13]
	v_mov_b32_e32 v0, 0x20000
	s_waitcnt lgkmcnt(0)
	s_barrier
	ds_read_b96 v[186:188], v0
	v_lshlrev_b32_e32 v0, 10, v193
	s_load_dwordx4 s[12:15], s[0:1], 0x8
	v_and_b32_e32 v0, 0xc00, v0
	v_lshlrev_b32_e32 v1, 1, v193
	s_waitcnt lgkmcnt(0)
	v_readfirstlane_b32 s18, v188
	s_lshl_b32 s2, s18, 5
	v_add_u32_e32 v0, s2, v0
	v_bfe_u32 v109, v193, 4, 2
	v_and_or_b32 v0, v1, 24, v0
	s_lshr_b32 s3, s3, 6
	v_lshlrev_b32_e32 v217, 3, v109
	v_ashrrev_i32_e32 v1, 31, v0
	v_lshl_or_b32 v200, s3, 8, v217
	v_lshlrev_b64 v[4:5], 2, v[0:1]
	v_mov_b32_e32 v201, 0
	v_lshl_add_u64 v[6:7], s[14:15], 0, v[4:5]
	v_lshlrev_b64 v[0:1], 14, v[200:201]
	v_lshl_add_u64 v[0:1], v[6:7], 0, v[0:1]
	global_load_dwordx4 v[8:11], v[0:1], off offset:16
	global_load_dwordx4 v[12:15], v[0:1], off
	v_or_b32_e32 v0, 1, v200
	v_mov_b32_e32 v1, v201
	v_lshlrev_b64 v[0:1], 14, v[0:1]
	v_lshl_add_u64 v[0:1], v[6:7], 0, v[0:1]
	global_load_dwordx4 v[16:19], v[0:1], off offset:16
	global_load_dwordx4 v[20:23], v[0:1], off
	v_or_b32_e32 v0, 2, v200
	v_mov_b32_e32 v1, v201
	v_lshlrev_b64 v[0:1], 14, v[0:1]
	v_lshl_add_u64 v[0:1], v[6:7], 0, v[0:1]
	global_load_dwordx4 v[24:27], v[0:1], off offset:16
	global_load_dwordx4 v[28:31], v[0:1], off
	v_or_b32_e32 v0, 3, v200
	v_mov_b32_e32 v1, v201
	v_lshlrev_b64 v[0:1], 14, v[0:1]
	v_lshl_add_u64 v[0:1], v[6:7], 0, v[0:1]
	global_load_dwordx4 v[32:35], v[0:1], off offset:16
	global_load_dwordx4 v[36:39], v[0:1], off
	v_or_b32_e32 v0, 4, v200
	v_mov_b32_e32 v1, v201
	v_lshlrev_b64 v[0:1], 14, v[0:1]
	v_lshl_add_u64 v[0:1], v[6:7], 0, v[0:1]
	global_load_dwordx4 v[40:43], v[0:1], off offset:16
	global_load_dwordx4 v[44:47], v[0:1], off
	v_or_b32_e32 v0, 5, v200
	v_mov_b32_e32 v1, v201
	v_lshlrev_b64 v[0:1], 14, v[0:1]
	v_lshl_add_u64 v[0:1], v[6:7], 0, v[0:1]
	global_load_dwordx4 v[48:51], v[0:1], off offset:16
	global_load_dwordx4 v[52:55], v[0:1], off
	v_or_b32_e32 v0, 6, v200
	v_mov_b32_e32 v1, v201
	v_lshlrev_b64 v[0:1], 14, v[0:1]
	v_lshl_add_u64 v[0:1], v[6:7], 0, v[0:1]
	global_load_dwordx4 v[56:59], v[0:1], off offset:16
	global_load_dwordx4 v[60:63], v[0:1], off
	v_or_b32_e32 v0, 7, v200
	v_mov_b32_e32 v1, v201
	v_lshlrev_b64 v[0:1], 14, v[0:1]
	v_lshl_add_u64 v[0:1], v[6:7], 0, v[0:1]
	global_load_dwordx4 v[64:67], v[0:1], off offset:16
	global_load_dwordx4 v[68:71], v[0:1], off
	v_mov_b32_e32 v1, v201
	s_lshl_b32 s14, s3, 7
	v_and_b32_e32 v198, 63, v193
	v_lshlrev_b32_e32 v108, 4, v198
	v_lshl_or_b32 v95, s3, 15, v108
	s_lshl_b32 s0, s3, 11
	v_bfe_u32 v207, v193, 3, 3
	s_lshl_b32 s20, s3, 3
	v_or_b32_e32 v208, s20, v207
	v_readfirstlane_b32 s19, v187
	v_and_b32_e32 v150, 7, v193
	s_mov_b32 s15, 0
	v_or_b32_e32 v198, s0, v198
	s_mov_b32 s24, s15
	s_mov_b32 s25, s15
	s_mov_b32 s26, s15
	s_mov_b32 s27, s15
	v_and_b32_e32 v220, 15, v193
	s_lshl_b32 s22, s18, 2
	s_add_i32 s22, s22, s3
	s_lshl_b32 s21, s3, 12
	s_and_b32 s3, s22, 7
	s_ashr_i32 s23, s22, 3
	s_and_b32 s9, s9, 0xffff
	s_add_i32 s23, s23, 16
	v_mov_b32_e32 v202, v201
	v_mov_b32_e32 v203, v201
	s_mov_b32 s11, 0x20000
	s_mov_b32 s10, 0x40000
	s_waitcnt vmcnt(12)
	v_cvt_pk_f16_f32 v231, v12, v20
	v_accvgpr_write_b32 a0, v231
	s_waitcnt vmcnt(8)
	v_cvt_pk_f16_f32 v230, v28, v36
	v_accvgpr_write_b32 a1, v230
	s_waitcnt vmcnt(4)
	v_cvt_pk_f16_f32 v229, v44, v52
	v_accvgpr_write_b32 a2, v229
	s_waitcnt vmcnt(1)
	v_cvt_pk_f16_f32 v0, v56, v64
	v_accvgpr_write_b32 a131, v0
	v_cvt_pk_f16_f32 v0, v40, v48
	v_accvgpr_write_b32 a130, v0
	v_cvt_pk_f16_f32 v0, v24, v32
	v_accvgpr_write_b32 a129, v0
	v_cvt_pk_f16_f32 v0, v8, v16
	v_accvgpr_write_b32 a128, v0
	s_waitcnt vmcnt(0)
	v_cvt_pk_f16_f32 v0, v61, v69
	v_accvgpr_write_b32 a35, v0
	v_cvt_pk_f16_f32 v0, v45, v53
	v_accvgpr_write_b32 a34, v0
	v_cvt_pk_f16_f32 v0, v29, v37
	v_accvgpr_write_b32 a33, v0
	v_cvt_pk_f16_f32 v0, v13, v21
	v_accvgpr_write_b32 a32, v0
	v_cvt_pk_f16_f32 v0, v57, v65
	v_accvgpr_write_b32 a163, v0
	v_cvt_pk_f16_f32 v0, v41, v49
	v_accvgpr_write_b32 a162, v0
	v_cvt_pk_f16_f32 v0, v25, v33
	v_accvgpr_write_b32 a161, v0
	v_cvt_pk_f16_f32 v0, v9, v17
	v_accvgpr_write_b32 a160, v0
	v_cvt_pk_f16_f32 v0, v62, v70
	v_accvgpr_write_b32 a67, v0
	v_cvt_pk_f16_f32 v0, v46, v54
	v_accvgpr_write_b32 a66, v0
	v_cvt_pk_f16_f32 v0, v30, v38
	v_accvgpr_write_b32 a65, v0
	v_cvt_pk_f16_f32 v0, v14, v22
	v_accvgpr_write_b32 a64, v0
	v_cvt_pk_f16_f32 v0, v58, v66
	v_accvgpr_write_b32 a195, v0
	v_cvt_pk_f16_f32 v0, v42, v50
	v_accvgpr_write_b32 a194, v0
	v_cvt_pk_f16_f32 v0, v26, v34
	v_accvgpr_write_b32 a193, v0
	v_cvt_pk_f16_f32 v0, v10, v18
	v_accvgpr_write_b32 a192, v0
	v_cvt_pk_f16_f32 v0, v63, v71
	v_accvgpr_write_b32 a99, v0
	v_cvt_pk_f16_f32 v0, v47, v55
	v_accvgpr_write_b32 a98, v0
	v_cvt_pk_f16_f32 v0, v31, v39
	v_accvgpr_write_b32 a97, v0
	v_cvt_pk_f16_f32 v0, v15, v23
	v_accvgpr_write_b32 a96, v0
	v_cvt_pk_f16_f32 v0, v59, v67
	v_accvgpr_write_b32 a227, v0
	v_cvt_pk_f16_f32 v0, v43, v51
	v_accvgpr_write_b32 a226, v0
	v_cvt_pk_f16_f32 v0, v27, v35
	v_accvgpr_write_b32 a225, v0
	v_cvt_pk_f16_f32 v0, v11, v19
	v_accvgpr_write_b32 a224, v0
	v_or_b32_e32 v0, 32, v200
	v_lshlrev_b64 v[0:1], 14, v[0:1]
	v_lshl_add_u64 v[0:1], v[6:7], 0, v[0:1]
	global_load_dwordx4 v[8:11], v[0:1], off offset:16
	global_load_dwordx4 v[12:15], v[0:1], off
	v_or_b32_e32 v0, 33, v200
	v_mov_b32_e32 v1, v201
	v_lshlrev_b64 v[0:1], 14, v[0:1]
	v_lshl_add_u64 v[0:1], v[6:7], 0, v[0:1]
	global_load_dwordx4 v[16:19], v[0:1], off offset:16
	global_load_dwordx4 v[20:23], v[0:1], off
	v_or_b32_e32 v0, 34, v200
	v_mov_b32_e32 v1, v201
	v_lshlrev_b64 v[0:1], 14, v[0:1]
	v_lshl_add_u64 v[0:1], v[6:7], 0, v[0:1]
	global_load_dwordx4 v[24:27], v[0:1], off offset:16
	global_load_dwordx4 v[28:31], v[0:1], off
	v_or_b32_e32 v0, 35, v200
	v_mov_b32_e32 v1, v201
	v_lshlrev_b64 v[0:1], 14, v[0:1]
	v_lshl_add_u64 v[0:1], v[6:7], 0, v[0:1]
	global_load_dwordx4 v[32:35], v[0:1], off offset:16
	global_load_dwordx4 v[36:39], v[0:1], off
	v_or_b32_e32 v0, 36, v200
	v_mov_b32_e32 v1, v201
	v_lshlrev_b64 v[0:1], 14, v[0:1]
	v_lshl_add_u64 v[0:1], v[6:7], 0, v[0:1]
	global_load_dwordx4 v[40:43], v[0:1], off offset:16
	global_load_dwordx4 v[44:47], v[0:1], off
	v_or_b32_e32 v0, 37, v200
	v_mov_b32_e32 v1, v201
	v_lshlrev_b64 v[0:1], 14, v[0:1]
	v_lshl_add_u64 v[0:1], v[6:7], 0, v[0:1]
	global_load_dwordx4 v[48:51], v[0:1], off offset:16
	global_load_dwordx4 v[52:55], v[0:1], off
	v_or_b32_e32 v0, 38, v200
	v_mov_b32_e32 v1, v201
	v_lshlrev_b64 v[0:1], 14, v[0:1]
	v_lshl_add_u64 v[0:1], v[6:7], 0, v[0:1]
	v_cvt_pk_f16_f32 v228, v60, v68
	global_load_dwordx4 v[56:59], v[0:1], off offset:16
	global_load_dwordx4 v[60:63], v[0:1], off
	v_or_b32_e32 v0, 39, v200
	v_mov_b32_e32 v1, v201
	v_lshlrev_b64 v[0:1], 14, v[0:1]
	v_lshl_add_u64 v[0:1], v[6:7], 0, v[0:1]
	global_load_dwordx4 v[64:67], v[0:1], off offset:16
	global_load_dwordx4 v[68:71], v[0:1], off
	v_mov_b32_e32 v1, v201
	v_accvgpr_write_b32 a3, v228
	s_waitcnt vmcnt(12)
	v_cvt_pk_f16_f32 v206, v12, v20
	v_accvgpr_write_b32 a4, v206
	s_waitcnt vmcnt(8)
	v_cvt_pk_f16_f32 v197, v28, v36
	v_accvgpr_write_b32 a5, v197
	s_waitcnt vmcnt(4)
	v_cvt_pk_f16_f32 v199, v44, v52
	v_accvgpr_write_b32 a6, v199
	s_waitcnt vmcnt(1)
	v_cvt_pk_f16_f32 v0, v56, v64
	v_accvgpr_write_b32 a135, v0
	v_cvt_pk_f16_f32 v0, v40, v48
	v_accvgpr_write_b32 a134, v0
	v_cvt_pk_f16_f32 v0, v24, v32
	v_accvgpr_write_b32 a133, v0
	v_cvt_pk_f16_f32 v0, v8, v16
	v_accvgpr_write_b32 a132, v0
	s_waitcnt vmcnt(0)
	v_cvt_pk_f16_f32 v0, v61, v69
	v_accvgpr_write_b32 a39, v0
	v_cvt_pk_f16_f32 v0, v45, v53
	v_accvgpr_write_b32 a38, v0
	v_cvt_pk_f16_f32 v0, v29, v37
	v_accvgpr_write_b32 a37, v0
	v_cvt_pk_f16_f32 v0, v13, v21
	v_accvgpr_write_b32 a36, v0
	v_cvt_pk_f16_f32 v0, v57, v65
	v_accvgpr_write_b32 a167, v0
	v_cvt_pk_f16_f32 v0, v41, v49
	v_accvgpr_write_b32 a166, v0
	v_cvt_pk_f16_f32 v0, v25, v33
	v_accvgpr_write_b32 a165, v0
	v_cvt_pk_f16_f32 v0, v9, v17
	v_accvgpr_write_b32 a164, v0
	v_cvt_pk_f16_f32 v0, v62, v70
	v_accvgpr_write_b32 a71, v0
	v_cvt_pk_f16_f32 v0, v46, v54
	v_accvgpr_write_b32 a70, v0
	v_cvt_pk_f16_f32 v0, v30, v38
	v_accvgpr_write_b32 a69, v0
	v_cvt_pk_f16_f32 v0, v14, v22
	v_accvgpr_write_b32 a68, v0
	v_cvt_pk_f16_f32 v0, v58, v66
	v_accvgpr_write_b32 a199, v0
	v_cvt_pk_f16_f32 v0, v42, v50
	v_accvgpr_write_b32 a198, v0
	v_cvt_pk_f16_f32 v0, v26, v34
	v_accvgpr_write_b32 a197, v0
	v_cvt_pk_f16_f32 v0, v10, v18
	v_accvgpr_write_b32 a196, v0
	v_cvt_pk_f16_f32 v0, v63, v71
	v_accvgpr_write_b32 a103, v0
	v_cvt_pk_f16_f32 v0, v47, v55
	v_accvgpr_write_b32 a102, v0
	v_cvt_pk_f16_f32 v0, v31, v39
	v_accvgpr_write_b32 a101, v0
	v_cvt_pk_f16_f32 v0, v15, v23
	v_accvgpr_write_b32 a100, v0
	v_cvt_pk_f16_f32 v0, v59, v67
	v_accvgpr_write_b32 a231, v0
	v_cvt_pk_f16_f32 v0, v43, v51
	v_accvgpr_write_b32 a230, v0
	v_cvt_pk_f16_f32 v0, v27, v35
	v_accvgpr_write_b32 a229, v0
	v_cvt_pk_f16_f32 v0, v11, v19
	v_accvgpr_write_b32 a228, v0
	v_or_b32_e32 v0, 64, v200
	v_lshlrev_b64 v[0:1], 14, v[0:1]
	v_lshl_add_u64 v[0:1], v[6:7], 0, v[0:1]
	global_load_dwordx4 v[8:11], v[0:1], off offset:16
	global_load_dwordx4 v[12:15], v[0:1], off
	v_or_b32_e32 v0, 0x41, v200
	v_mov_b32_e32 v1, v201
	v_lshlrev_b64 v[0:1], 14, v[0:1]
	v_lshl_add_u64 v[0:1], v[6:7], 0, v[0:1]
	global_load_dwordx4 v[16:19], v[0:1], off offset:16
	global_load_dwordx4 v[20:23], v[0:1], off
	v_or_b32_e32 v0, 0x42, v200
	v_mov_b32_e32 v1, v201
	v_lshlrev_b64 v[0:1], 14, v[0:1]
	v_lshl_add_u64 v[0:1], v[6:7], 0, v[0:1]
	global_load_dwordx4 v[24:27], v[0:1], off offset:16
	global_load_dwordx4 v[28:31], v[0:1], off
	v_or_b32_e32 v0, 0x43, v200
	v_mov_b32_e32 v1, v201
	v_lshlrev_b64 v[0:1], 14, v[0:1]
	v_lshl_add_u64 v[0:1], v[6:7], 0, v[0:1]
	global_load_dwordx4 v[32:35], v[0:1], off offset:16
	global_load_dwordx4 v[36:39], v[0:1], off
	v_or_b32_e32 v0, 0x44, v200
	v_mov_b32_e32 v1, v201
	v_lshlrev_b64 v[0:1], 14, v[0:1]
	v_lshl_add_u64 v[0:1], v[6:7], 0, v[0:1]
	global_load_dwordx4 v[40:43], v[0:1], off offset:16
	global_load_dwordx4 v[44:47], v[0:1], off
	v_or_b32_e32 v0, 0x45, v200
	v_mov_b32_e32 v1, v201
	v_lshlrev_b64 v[0:1], 14, v[0:1]
	v_lshl_add_u64 v[0:1], v[6:7], 0, v[0:1]
	global_load_dwordx4 v[48:51], v[0:1], off offset:16
	global_load_dwordx4 v[52:55], v[0:1], off
	v_or_b32_e32 v0, 0x46, v200
	v_mov_b32_e32 v1, v201
	v_lshlrev_b64 v[0:1], 14, v[0:1]
	v_lshl_add_u64 v[0:1], v[6:7], 0, v[0:1]
	v_cvt_pk_f16_f32 v205, v60, v68
	global_load_dwordx4 v[56:59], v[0:1], off offset:16
	global_load_dwordx4 v[60:63], v[0:1], off
	v_or_b32_e32 v0, 0x47, v200
	v_mov_b32_e32 v1, v201
	v_lshlrev_b64 v[0:1], 14, v[0:1]
	v_lshl_add_u64 v[0:1], v[6:7], 0, v[0:1]
	global_load_dwordx4 v[64:67], v[0:1], off offset:16
	global_load_dwordx4 v[68:71], v[0:1], off
	v_mov_b32_e32 v1, v201
	v_accvgpr_write_b32 a7, v205
	s_waitcnt vmcnt(12)
	v_cvt_pk_f16_f32 v155, v12, v20
	v_accvgpr_write_b32 a8, v155
	s_waitcnt vmcnt(8)
	v_cvt_pk_f16_f32 v156, v28, v36
	v_accvgpr_write_b32 a9, v156
	s_waitcnt vmcnt(4)
	v_cvt_pk_f16_f32 v157, v44, v52
	v_accvgpr_write_b32 a10, v157
	s_waitcnt vmcnt(1)
	v_cvt_pk_f16_f32 v0, v56, v64
	v_accvgpr_write_b32 a139, v0
	v_cvt_pk_f16_f32 v0, v40, v48
	v_accvgpr_write_b32 a138, v0
	v_cvt_pk_f16_f32 v0, v24, v32
	v_accvgpr_write_b32 a137, v0
	v_cvt_pk_f16_f32 v0, v8, v16
	v_accvgpr_write_b32 a136, v0
	s_waitcnt vmcnt(0)
	v_cvt_pk_f16_f32 v0, v61, v69
	v_accvgpr_write_b32 a43, v0
	v_cvt_pk_f16_f32 v0, v45, v53
	v_accvgpr_write_b32 a42, v0
	v_cvt_pk_f16_f32 v0, v29, v37
	v_accvgpr_write_b32 a41, v0
	v_cvt_pk_f16_f32 v0, v13, v21
	v_accvgpr_write_b32 a40, v0
	v_cvt_pk_f16_f32 v0, v57, v65
	v_accvgpr_write_b32 a171, v0
	v_cvt_pk_f16_f32 v0, v41, v49
	v_accvgpr_write_b32 a170, v0
	v_cvt_pk_f16_f32 v0, v25, v33
	v_accvgpr_write_b32 a169, v0
	v_cvt_pk_f16_f32 v0, v9, v17
	v_accvgpr_write_b32 a168, v0
	v_cvt_pk_f16_f32 v0, v62, v70
	v_accvgpr_write_b32 a75, v0
	v_cvt_pk_f16_f32 v0, v46, v54
	v_accvgpr_write_b32 a74, v0
	v_cvt_pk_f16_f32 v0, v30, v38
	v_accvgpr_write_b32 a73, v0
	v_cvt_pk_f16_f32 v0, v14, v22
	v_accvgpr_write_b32 a72, v0
	v_cvt_pk_f16_f32 v0, v58, v66
	v_accvgpr_write_b32 a203, v0
	v_cvt_pk_f16_f32 v0, v42, v50
	v_accvgpr_write_b32 a202, v0
	v_cvt_pk_f16_f32 v0, v26, v34
	v_accvgpr_write_b32 a201, v0
	v_cvt_pk_f16_f32 v0, v10, v18
	v_accvgpr_write_b32 a200, v0
	v_cvt_pk_f16_f32 v0, v63, v71
	v_accvgpr_write_b32 a107, v0
	v_cvt_pk_f16_f32 v0, v47, v55
	v_accvgpr_write_b32 a106, v0
	v_cvt_pk_f16_f32 v0, v31, v39
	v_accvgpr_write_b32 a105, v0
	v_cvt_pk_f16_f32 v0, v15, v23
	v_accvgpr_write_b32 a104, v0
	v_cvt_pk_f16_f32 v0, v59, v67
	v_accvgpr_write_b32 a235, v0
	v_cvt_pk_f16_f32 v0, v43, v51
	v_accvgpr_write_b32 a234, v0
	v_cvt_pk_f16_f32 v0, v27, v35
	v_accvgpr_write_b32 a233, v0
	v_cvt_pk_f16_f32 v0, v11, v19
	v_accvgpr_write_b32 a232, v0
	v_or_b32_e32 v0, 0x60, v200
	v_lshlrev_b64 v[0:1], 14, v[0:1]
	v_lshl_add_u64 v[0:1], v[6:7], 0, v[0:1]
	global_load_dwordx4 v[8:11], v[0:1], off offset:16
	global_load_dwordx4 v[12:15], v[0:1], off
	v_or_b32_e32 v0, 0x61, v200
	v_mov_b32_e32 v1, v201
	v_lshlrev_b64 v[0:1], 14, v[0:1]
	v_lshl_add_u64 v[0:1], v[6:7], 0, v[0:1]
	global_load_dwordx4 v[16:19], v[0:1], off offset:16
	global_load_dwordx4 v[20:23], v[0:1], off
	v_or_b32_e32 v0, 0x62, v200
	v_mov_b32_e32 v1, v201
	v_lshlrev_b64 v[0:1], 14, v[0:1]
	v_lshl_add_u64 v[0:1], v[6:7], 0, v[0:1]
	global_load_dwordx4 v[24:27], v[0:1], off offset:16
	global_load_dwordx4 v[28:31], v[0:1], off
	v_or_b32_e32 v0, 0x63, v200
	v_mov_b32_e32 v1, v201
	v_lshlrev_b64 v[0:1], 14, v[0:1]
	v_lshl_add_u64 v[0:1], v[6:7], 0, v[0:1]
	global_load_dwordx4 v[32:35], v[0:1], off offset:16
	global_load_dwordx4 v[36:39], v[0:1], off
	v_or_b32_e32 v0, 0x64, v200
	v_mov_b32_e32 v1, v201
	v_lshlrev_b64 v[0:1], 14, v[0:1]
	v_lshl_add_u64 v[0:1], v[6:7], 0, v[0:1]
	global_load_dwordx4 v[40:43], v[0:1], off offset:16
	global_load_dwordx4 v[44:47], v[0:1], off
	v_or_b32_e32 v0, 0x65, v200
	v_mov_b32_e32 v1, v201
	v_lshlrev_b64 v[0:1], 14, v[0:1]
	v_lshl_add_u64 v[0:1], v[6:7], 0, v[0:1]
	global_load_dwordx4 v[48:51], v[0:1], off offset:16
	global_load_dwordx4 v[52:55], v[0:1], off
	v_or_b32_e32 v0, 0x66, v200
	v_mov_b32_e32 v1, v201
	v_lshlrev_b64 v[0:1], 14, v[0:1]
	v_lshl_add_u64 v[0:1], v[6:7], 0, v[0:1]
	v_cvt_pk_f16_f32 v158, v60, v68
	global_load_dwordx4 v[56:59], v[0:1], off offset:16
	global_load_dwordx4 v[60:63], v[0:1], off
	v_or_b32_e32 v0, 0x67, v200
	v_mov_b32_e32 v1, v201
	v_lshlrev_b64 v[0:1], 14, v[0:1]
	v_lshl_add_u64 v[0:1], v[6:7], 0, v[0:1]
	global_load_dwordx4 v[64:67], v[0:1], off offset:16
	global_load_dwordx4 v[68:71], v[0:1], off
	v_mov_b32_e32 v1, v201
	v_accvgpr_write_b32 a11, v158
	s_waitcnt vmcnt(12)
	v_cvt_pk_f16_f32 v122, v12, v20
	v_accvgpr_write_b32 a12, v122
	s_waitcnt vmcnt(8)
	v_cvt_pk_f16_f32 v123, v28, v36
	v_accvgpr_write_b32 a13, v123
	s_waitcnt vmcnt(4)
	v_cvt_pk_f16_f32 v124, v44, v52
	v_accvgpr_write_b32 a14, v124
	s_waitcnt vmcnt(1)
	v_cvt_pk_f16_f32 v0, v56, v64
	v_accvgpr_write_b32 a143, v0
	v_cvt_pk_f16_f32 v0, v40, v48
	v_accvgpr_write_b32 a142, v0
	v_cvt_pk_f16_f32 v0, v24, v32
	v_accvgpr_write_b32 a141, v0
	v_cvt_pk_f16_f32 v0, v8, v16
	v_accvgpr_write_b32 a140, v0
	s_waitcnt vmcnt(0)
	v_cvt_pk_f16_f32 v0, v61, v69
	v_accvgpr_write_b32 a47, v0
	v_cvt_pk_f16_f32 v0, v45, v53
	v_accvgpr_write_b32 a46, v0
	v_cvt_pk_f16_f32 v0, v29, v37
	v_accvgpr_write_b32 a45, v0
	v_cvt_pk_f16_f32 v0, v13, v21
	v_accvgpr_write_b32 a44, v0
	v_cvt_pk_f16_f32 v0, v57, v65
	v_accvgpr_write_b32 a175, v0
	v_cvt_pk_f16_f32 v0, v41, v49
	v_accvgpr_write_b32 a174, v0
	v_cvt_pk_f16_f32 v0, v25, v33
	v_accvgpr_write_b32 a173, v0
	v_cvt_pk_f16_f32 v0, v9, v17
	v_accvgpr_write_b32 a172, v0
	v_cvt_pk_f16_f32 v0, v62, v70
	v_accvgpr_write_b32 a79, v0
	v_cvt_pk_f16_f32 v0, v46, v54
	v_accvgpr_write_b32 a78, v0
	v_cvt_pk_f16_f32 v0, v30, v38
	v_accvgpr_write_b32 a77, v0
	v_cvt_pk_f16_f32 v0, v14, v22
	v_accvgpr_write_b32 a76, v0
	v_cvt_pk_f16_f32 v0, v58, v66
	v_accvgpr_write_b32 a207, v0
	v_cvt_pk_f16_f32 v0, v42, v50
	v_accvgpr_write_b32 a206, v0
	v_cvt_pk_f16_f32 v0, v26, v34
	v_accvgpr_write_b32 a205, v0
	v_cvt_pk_f16_f32 v0, v10, v18
	v_accvgpr_write_b32 a204, v0
	v_cvt_pk_f16_f32 v0, v63, v71
	v_accvgpr_write_b32 a111, v0
	v_cvt_pk_f16_f32 v0, v47, v55
	v_accvgpr_write_b32 a110, v0
	v_cvt_pk_f16_f32 v0, v31, v39
	v_accvgpr_write_b32 a109, v0
	v_cvt_pk_f16_f32 v0, v15, v23
	v_accvgpr_write_b32 a108, v0
	v_cvt_pk_f16_f32 v0, v59, v67
	v_accvgpr_write_b32 a239, v0
	v_cvt_pk_f16_f32 v0, v43, v51
	v_accvgpr_write_b32 a238, v0
	v_cvt_pk_f16_f32 v0, v27, v35
	v_accvgpr_write_b32 a237, v0
	v_cvt_pk_f16_f32 v0, v11, v19
	v_accvgpr_write_b32 a236, v0
	v_or_b32_e32 v0, 0x80, v200
	v_lshlrev_b64 v[0:1], 14, v[0:1]
	v_lshl_add_u64 v[0:1], v[6:7], 0, v[0:1]
	global_load_dwordx4 v[8:11], v[0:1], off offset:16
	global_load_dwordx4 v[12:15], v[0:1], off
	v_or_b32_e32 v0, 0x81, v200
	v_mov_b32_e32 v1, v201
	v_lshlrev_b64 v[0:1], 14, v[0:1]
	v_lshl_add_u64 v[0:1], v[6:7], 0, v[0:1]
	global_load_dwordx4 v[16:19], v[0:1], off offset:16
	global_load_dwordx4 v[20:23], v[0:1], off
	v_or_b32_e32 v0, 0x82, v200
	v_mov_b32_e32 v1, v201
	v_lshlrev_b64 v[0:1], 14, v[0:1]
	v_lshl_add_u64 v[0:1], v[6:7], 0, v[0:1]
	global_load_dwordx4 v[24:27], v[0:1], off offset:16
	global_load_dwordx4 v[28:31], v[0:1], off
	v_or_b32_e32 v0, 0x83, v200
	v_mov_b32_e32 v1, v201
	v_lshlrev_b64 v[0:1], 14, v[0:1]
	v_lshl_add_u64 v[0:1], v[6:7], 0, v[0:1]
	global_load_dwordx4 v[32:35], v[0:1], off offset:16
	global_load_dwordx4 v[36:39], v[0:1], off
	v_or_b32_e32 v0, 0x84, v200
	v_mov_b32_e32 v1, v201
	v_lshlrev_b64 v[0:1], 14, v[0:1]
	v_lshl_add_u64 v[0:1], v[6:7], 0, v[0:1]
	global_load_dwordx4 v[40:43], v[0:1], off offset:16
	global_load_dwordx4 v[44:47], v[0:1], off
	v_or_b32_e32 v0, 0x85, v200
	v_mov_b32_e32 v1, v201
	v_lshlrev_b64 v[0:1], 14, v[0:1]
	v_lshl_add_u64 v[0:1], v[6:7], 0, v[0:1]
	global_load_dwordx4 v[48:51], v[0:1], off offset:16
	global_load_dwordx4 v[52:55], v[0:1], off
	v_or_b32_e32 v0, 0x86, v200
	v_mov_b32_e32 v1, v201
	v_lshlrev_b64 v[0:1], 14, v[0:1]
	v_lshl_add_u64 v[0:1], v[6:7], 0, v[0:1]
	v_cvt_pk_f16_f32 v125, v60, v68
	global_load_dwordx4 v[56:59], v[0:1], off offset:16
	global_load_dwordx4 v[60:63], v[0:1], off
	v_or_b32_e32 v0, 0x87, v200
	v_mov_b32_e32 v1, v201
	v_lshlrev_b64 v[0:1], 14, v[0:1]
	v_lshl_add_u64 v[0:1], v[6:7], 0, v[0:1]
	global_load_dwordx4 v[64:67], v[0:1], off offset:16
	global_load_dwordx4 v[68:71], v[0:1], off
	v_mov_b32_e32 v1, v201
	v_accvgpr_write_b32 a15, v125
	s_waitcnt vmcnt(12)
	v_cvt_pk_f16_f32 v114, v12, v20
	v_cvt_pk_f16_f32 v245, v13, v21
	v_cvt_pk_f16_f32 v235, v14, v22
	v_cvt_pk_f16_f32 v227, v15, v23
	v_accvgpr_write_b32 a16, v114
	v_accvgpr_write_b32 a48, v245
	v_accvgpr_write_b32 a80, v235
	v_accvgpr_write_b32 a112, v227
	s_waitcnt vmcnt(8)
	v_cvt_pk_f16_f32 v115, v28, v36
	v_cvt_pk_f16_f32 v243, v29, v37
	v_cvt_pk_f16_f32 v234, v30, v38
	v_cvt_pk_f16_f32 v226, v31, v39
	v_accvgpr_write_b32 a17, v115
	v_accvgpr_write_b32 a49, v243
	v_accvgpr_write_b32 a81, v234
	v_accvgpr_write_b32 a113, v226
	s_waitcnt vmcnt(4)
	v_cvt_pk_f16_f32 v116, v44, v52
	v_cvt_pk_f16_f32 v241, v45, v53
	v_cvt_pk_f16_f32 v233, v46, v54
	v_cvt_pk_f16_f32 v225, v47, v55
	v_accvgpr_write_b32 a18, v116
	v_accvgpr_write_b32 a50, v241
	v_accvgpr_write_b32 a82, v233
	v_accvgpr_write_b32 a114, v225
	s_waitcnt vmcnt(1)
	v_cvt_pk_f16_f32 v0, v56, v64
	v_accvgpr_write_b32 a147, v0
	v_cvt_pk_f16_f32 v0, v40, v48
	v_accvgpr_write_b32 a146, v0
	v_cvt_pk_f16_f32 v0, v24, v32
	v_accvgpr_write_b32 a145, v0
	v_cvt_pk_f16_f32 v0, v8, v16
	v_accvgpr_write_b32 a144, v0
	v_cvt_pk_f16_f32 v0, v57, v65
	v_accvgpr_write_b32 a179, v0
	v_cvt_pk_f16_f32 v0, v41, v49
	v_accvgpr_write_b32 a178, v0
	v_cvt_pk_f16_f32 v0, v25, v33
	v_accvgpr_write_b32 a177, v0
	v_cvt_pk_f16_f32 v0, v9, v17
	v_accvgpr_write_b32 a176, v0
	v_cvt_pk_f16_f32 v0, v58, v66
	v_accvgpr_write_b32 a211, v0
	v_cvt_pk_f16_f32 v0, v42, v50
	v_accvgpr_write_b32 a210, v0
	v_cvt_pk_f16_f32 v0, v26, v34
	v_accvgpr_write_b32 a209, v0
	v_cvt_pk_f16_f32 v0, v10, v18
	v_accvgpr_write_b32 a208, v0
	s_waitcnt vmcnt(0)
	v_cvt_pk_f16_f32 v0, v63, v71
	v_accvgpr_write_b32 a115, v0
	v_cvt_pk_f16_f32 v0, v59, v67
	v_accvgpr_write_b32 a243, v0
	v_cvt_pk_f16_f32 v0, v43, v51
	v_accvgpr_write_b32 a242, v0
	v_cvt_pk_f16_f32 v0, v27, v35
	v_accvgpr_write_b32 a241, v0
	v_cvt_pk_f16_f32 v0, v11, v19
	v_accvgpr_write_b32 a240, v0
	v_or_b32_e32 v0, 0xa0, v200
	v_lshlrev_b64 v[0:1], 14, v[0:1]
	v_lshl_add_u64 v[0:1], v[6:7], 0, v[0:1]
	global_load_dwordx4 v[8:11], v[0:1], off offset:16
	global_load_dwordx4 v[12:15], v[0:1], off
	v_or_b32_e32 v0, 0xa1, v200
	v_mov_b32_e32 v1, v201
	v_lshlrev_b64 v[0:1], 14, v[0:1]
	v_lshl_add_u64 v[0:1], v[6:7], 0, v[0:1]
	global_load_dwordx4 v[16:19], v[0:1], off offset:16
	global_load_dwordx4 v[20:23], v[0:1], off
	v_or_b32_e32 v0, 0xa2, v200
	v_mov_b32_e32 v1, v201
	v_lshlrev_b64 v[0:1], 14, v[0:1]
	v_lshl_add_u64 v[0:1], v[6:7], 0, v[0:1]
	global_load_dwordx4 v[24:27], v[0:1], off offset:16
	global_load_dwordx4 v[28:31], v[0:1], off
	v_or_b32_e32 v0, 0xa3, v200
	v_mov_b32_e32 v1, v201
	v_lshlrev_b64 v[0:1], 14, v[0:1]
	v_lshl_add_u64 v[0:1], v[6:7], 0, v[0:1]
	global_load_dwordx4 v[32:35], v[0:1], off offset:16
	global_load_dwordx4 v[36:39], v[0:1], off
	v_or_b32_e32 v0, 0xa4, v200
	v_mov_b32_e32 v1, v201
	v_lshlrev_b64 v[0:1], 14, v[0:1]
	v_lshl_add_u64 v[0:1], v[6:7], 0, v[0:1]
	global_load_dwordx4 v[40:43], v[0:1], off offset:16
	global_load_dwordx4 v[44:47], v[0:1], off
	v_or_b32_e32 v0, 0xa5, v200
	v_mov_b32_e32 v1, v201
	v_lshlrev_b64 v[0:1], 14, v[0:1]
	v_lshl_add_u64 v[0:1], v[6:7], 0, v[0:1]
	global_load_dwordx4 v[48:51], v[0:1], off offset:16
	global_load_dwordx4 v[52:55], v[0:1], off
	v_or_b32_e32 v0, 0xa6, v200
	v_mov_b32_e32 v1, v201
	v_lshlrev_b64 v[0:1], 14, v[0:1]
	v_lshl_add_u64 v[0:1], v[6:7], 0, v[0:1]
	v_cvt_pk_f16_f32 v117, v60, v68
	v_cvt_pk_f16_f32 v240, v61, v69
	v_cvt_pk_f16_f32 v232, v62, v70
	global_load_dwordx4 v[56:59], v[0:1], off offset:16
	global_load_dwordx4 v[60:63], v[0:1], off
	v_or_b32_e32 v0, 0xa7, v200
	v_mov_b32_e32 v1, v201
	v_lshlrev_b64 v[0:1], 14, v[0:1]
	v_lshl_add_u64 v[0:1], v[6:7], 0, v[0:1]
	global_load_dwordx4 v[64:67], v[0:1], off offset:16
	global_load_dwordx4 v[68:71], v[0:1], off
	v_or_b32_e32 v0, 0xc0, v200
	v_mov_b32_e32 v1, v201
	v_lshlrev_b64 v[0:1], 14, v[0:1]
	v_lshl_add_u64 v[0:1], v[6:7], 0, v[0:1]
	v_accvgpr_write_b32 a19, v117
	v_accvgpr_write_b32 a51, v240
	v_accvgpr_write_b32 a83, v232
	s_waitcnt vmcnt(13)
	v_cvt_pk_f16_f32 v255, v8, v16
	s_waitcnt vmcnt(12)
	v_cvt_pk_f16_f32 v110, v12, v20
	v_cvt_pk_f16_f32 v204, v13, v21
	v_cvt_pk_f16_f32 v251, v9, v17
	v_cvt_pk_f16_f32 v196, v14, v22
	v_cvt_pk_f16_f32 v247, v10, v18
	v_cvt_pk_f16_f32 v212, v15, v23
	v_cvt_pk_f16_f32 v239, v11, v19
	global_load_dwordx4 v[8:11], v[0:1], off offset:16
	global_load_dwordx4 v[12:15], v[0:1], off
	v_or_b32_e32 v0, 0xc1, v200
	v_mov_b32_e32 v1, v201
	v_lshlrev_b64 v[0:1], 14, v[0:1]
	v_lshl_add_u64 v[0:1], v[6:7], 0, v[0:1]
	global_load_dwordx4 v[16:19], v[0:1], off offset:16
	global_load_dwordx4 v[20:23], v[0:1], off
	v_or_b32_e32 v0, 0xc2, v200
	v_mov_b32_e32 v1, v201
	v_lshlrev_b64 v[0:1], 14, v[0:1]
	v_lshl_add_u64 v[0:1], v[6:7], 0, v[0:1]
	s_waitcnt vmcnt(12)
	v_cvt_pk_f16_f32 v111, v28, v36
	v_cvt_pk_f16_f32 v254, v24, v32
	v_cvt_pk_f16_f32 v180, v29, v37
	v_cvt_pk_f16_f32 v250, v25, v33
	v_cvt_pk_f16_f32 v213, v30, v38
	v_cvt_pk_f16_f32 v246, v26, v34
	v_cvt_pk_f16_f32 v216, v31, v39
	v_cvt_pk_f16_f32 v238, v27, v35
	global_load_dwordx4 v[24:27], v[0:1], off offset:16
	global_load_dwordx4 v[28:31], v[0:1], off
	v_or_b32_e32 v0, 0xc3, v200
	v_mov_b32_e32 v1, v201
	v_lshlrev_b64 v[0:1], 14, v[0:1]
	v_lshl_add_u64 v[0:1], v[6:7], 0, v[0:1]
	global_load_dwordx4 v[32:35], v[0:1], off offset:16
	global_load_dwordx4 v[36:39], v[0:1], off
	v_or_b32_e32 v0, 0xc4, v200
	v_mov_b32_e32 v1, v201
	v_lshlrev_b64 v[0:1], 14, v[0:1]
	v_lshl_add_u64 v[0:1], v[6:7], 0, v[0:1]
	s_waitcnt vmcnt(12)
	v_cvt_pk_f16_f32 v112, v44, v52
	v_cvt_pk_f16_f32 v253, v40, v48
	v_cvt_pk_f16_f32 v181, v45, v53
	v_cvt_pk_f16_f32 v249, v41, v49
	v_cvt_pk_f16_f32 v219, v46, v54
	v_cvt_pk_f16_f32 v244, v42, v50
	v_cvt_pk_f16_f32 v218, v47, v55
	v_cvt_pk_f16_f32 v237, v43, v51
	global_load_dwordx4 v[40:43], v[0:1], off offset:16
	global_load_dwordx4 v[44:47], v[0:1], off
	v_or_b32_e32 v0, 0xc5, v200
	v_mov_b32_e32 v1, v201
	v_lshlrev_b64 v[0:1], 14, v[0:1]
	v_lshl_add_u64 v[0:1], v[6:7], 0, v[0:1]
	global_load_dwordx4 v[48:51], v[0:1], off offset:16
	global_load_dwordx4 v[52:55], v[0:1], off
	v_or_b32_e32 v0, 0xc6, v200
	v_mov_b32_e32 v1, v201
	v_lshlrev_b64 v[0:1], 14, v[0:1]
	v_lshl_add_u64 v[0:1], v[6:7], 0, v[0:1]
	s_waitcnt vmcnt(12)
	v_cvt_pk_f16_f32 v113, v60, v68
	v_cvt_pk_f16_f32 v252, v56, v64
	v_cvt_pk_f16_f32 v183, v61, v69
	v_cvt_pk_f16_f32 v248, v57, v65
	v_cvt_pk_f16_f32 v222, v62, v70
	v_cvt_pk_f16_f32 v242, v58, v66
	v_cvt_pk_f16_f32 v221, v63, v71
	v_cvt_pk_f16_f32 v236, v59, v67
	global_load_dwordx4 v[56:59], v[0:1], off offset:16
	global_load_dwordx4 v[60:63], v[0:1], off
	v_or_b32_e32 v0, 0xc7, v200
	v_mov_b32_e32 v1, v201
	v_lshlrev_b64 v[0:1], 14, v[0:1]
	v_lshl_add_u64 v[0:1], v[6:7], 0, v[0:1]
	global_load_dwordx4 v[64:67], v[0:1], off offset:16
	global_load_dwordx4 v[68:71], v[0:1], off
	v_or_b32_e32 v0, 0xe0, v200
	v_mov_b32_e32 v1, v201
	v_lshlrev_b64 v[0:1], 14, v[0:1]
	v_lshl_add_u64 v[0:1], v[6:7], 0, v[0:1]
	v_accvgpr_write_b32 a20, v110
	v_accvgpr_write_b32 a21, v111
	v_accvgpr_write_b32 a22, v112
	v_accvgpr_write_b32 a23, v113
	v_accvgpr_write_b32 a52, v204
	v_accvgpr_write_b32 a53, v180
	v_accvgpr_write_b32 a54, v181
	v_accvgpr_write_b32 a55, v183
	v_accvgpr_write_b32 a84, v196
	v_accvgpr_write_b32 a85, v213
	v_accvgpr_write_b32 a86, v219
	v_accvgpr_write_b32 a87, v222
	v_accvgpr_write_b32 a116, v212
	v_accvgpr_write_b32 a117, v216
	v_accvgpr_write_b32 a118, v218
	v_accvgpr_write_b32 a119, v221
	v_accvgpr_write_b32 a148, v255
	v_accvgpr_write_b32 a149, v254
	v_accvgpr_write_b32 a150, v253
	v_accvgpr_write_b32 a151, v252
	s_waitcnt vmcnt(13)
	v_cvt_pk_f16_f32 v167, v8, v16
	s_waitcnt vmcnt(12)
	v_cvt_pk_f16_f32 v190, v12, v20
	v_cvt_pk_f16_f32 v146, v13, v21
	v_cvt_pk_f16_f32 v171, v9, v17
	v_cvt_pk_f16_f32 v159, v14, v22
	v_cvt_pk_f16_f32 v176, v10, v18
	v_cvt_pk_f16_f32 v163, v15, v23
	v_cvt_pk_f16_f32 v189, v11, v19
	global_load_dwordx4 v[8:11], v[0:1], off offset:16
	global_load_dwordx4 v[12:15], v[0:1], off
	v_or_b32_e32 v0, 0xe1, v200
	v_mov_b32_e32 v1, v201
	v_lshlrev_b64 v[0:1], 14, v[0:1]
	v_lshl_add_u64 v[0:1], v[6:7], 0, v[0:1]
	global_load_dwordx4 v[16:19], v[0:1], off offset:16
	global_load_dwordx4 v[20:23], v[0:1], off
	v_or_b32_e32 v0, 0xe2, v200
	v_mov_b32_e32 v1, v201
	v_lshlrev_b64 v[0:1], 14, v[0:1]
	v_lshl_add_u64 v[0:1], v[6:7], 0, v[0:1]
	s_waitcnt vmcnt(13)
	v_cvt_pk_f16_f32 v168, v24, v32
	s_waitcnt vmcnt(12)
	v_cvt_pk_f16_f32 v224, v28, v36
	v_cvt_pk_f16_f32 v147, v29, v37
	v_cvt_pk_f16_f32 v172, v25, v33
	v_cvt_pk_f16_f32 v160, v30, v38
	v_cvt_pk_f16_f32 v177, v26, v34
	v_cvt_pk_f16_f32 v164, v31, v39
	v_cvt_pk_f16_f32 v191, v27, v35
	global_load_dwordx4 v[24:27], v[0:1], off offset:16
	global_load_dwordx4 v[28:31], v[0:1], off
	v_or_b32_e32 v0, 0xe3, v200
	v_mov_b32_e32 v1, v201
	v_lshlrev_b64 v[0:1], 14, v[0:1]
	v_lshl_add_u64 v[0:1], v[6:7], 0, v[0:1]
	global_load_dwordx4 v[32:35], v[0:1], off offset:16
	global_load_dwordx4 v[36:39], v[0:1], off
	v_or_b32_e32 v0, 0xe4, v200
	v_mov_b32_e32 v1, v201
	v_lshlrev_b64 v[0:1], 14, v[0:1]
	v_lshl_add_u64 v[0:1], v[6:7], 0, v[0:1]
	s_waitcnt vmcnt(13)
	v_cvt_pk_f16_f32 v169, v40, v48
	s_waitcnt vmcnt(12)
	v_cvt_pk_f16_f32 v223, v44, v52
	v_cvt_pk_f16_f32 v148, v45, v53
	v_cvt_pk_f16_f32 v174, v41, v49
	v_cvt_pk_f16_f32 v161, v46, v54
	v_cvt_pk_f16_f32 v178, v42, v50
	v_cvt_pk_f16_f32 v165, v47, v55
	v_cvt_pk_f16_f32 v192, v43, v51
	global_load_dwordx4 v[40:43], v[0:1], off offset:16
	global_load_dwordx4 v[44:47], v[0:1], off
	v_or_b32_e32 v0, 0xe5, v200
	v_mov_b32_e32 v1, v201
	v_lshlrev_b64 v[0:1], 14, v[0:1]
	v_lshl_add_u64 v[0:1], v[6:7], 0, v[0:1]
	global_load_dwordx4 v[48:51], v[0:1], off offset:16
	global_load_dwordx4 v[52:55], v[0:1], off
	v_or_b32_e32 v0, 0xe6, v200
	v_mov_b32_e32 v1, v201
	v_lshlrev_b64 v[0:1], 14, v[0:1]
	v_lshl_add_u64 v[0:1], v[6:7], 0, v[0:1]
	v_or_b32_e32 v200, 0xe7, v200
	s_waitcnt vmcnt(12)
	v_cvt_pk_f16_f32 v194, v60, v68
	v_cvt_pk_f16_f32 v170, v56, v64
	v_cvt_pk_f16_f32 v149, v61, v69
	v_cvt_pk_f16_f32 v175, v57, v65
	v_cvt_pk_f16_f32 v162, v62, v70
	v_cvt_pk_f16_f32 v179, v58, v66
	v_cvt_pk_f16_f32 v166, v63, v71
	v_cvt_pk_f16_f32 v195, v59, v67
	global_load_dwordx4 v[56:59], v[0:1], off offset:16
	global_load_dwordx4 v[60:63], v[0:1], off
	v_lshlrev_b64 v[0:1], 14, v[200:201]
	v_lshl_add_u64 v[0:1], v[6:7], 0, v[0:1]
	global_load_dwordx4 v[64:67], v[0:1], off offset:16
	global_load_dwordx4 v[68:71], v[0:1], off
	v_or_b32_e32 v200, s14, v217
	v_lshlrev_b64 v[0:1], 14, v[200:201]
	v_accvgpr_write_b32 a24, v190
	v_accvgpr_write_b32 a25, v224
	v_accvgpr_write_b32 a26, v223
	v_accvgpr_write_b32 a27, v194
	v_accvgpr_write_b32 a56, v146
	v_accvgpr_write_b32 a57, v147
	v_accvgpr_write_b32 a58, v148
	v_accvgpr_write_b32 a59, v149
	v_accvgpr_write_b32 a88, v159
	v_accvgpr_write_b32 a89, v160
	v_accvgpr_write_b32 a90, v161
	v_accvgpr_write_b32 a91, v162
	v_accvgpr_write_b32 a120, v163
	v_accvgpr_write_b32 a121, v164
	v_accvgpr_write_b32 a122, v165
	v_accvgpr_write_b32 a123, v166
	v_accvgpr_write_b32 a152, v167
	v_accvgpr_write_b32 a153, v168
	v_accvgpr_write_b32 a154, v169
	v_accvgpr_write_b32 a155, v170
	v_accvgpr_write_b32 a180, v251
	v_accvgpr_write_b32 a181, v250
	v_accvgpr_write_b32 a182, v249
	s_waitcnt vmcnt(13)
	v_cvt_pk_f16_f32 v134, v8, v16
	v_cvt_pk_f16_f32 v138, v9, v17
	v_cvt_pk_f16_f32 v142, v10, v18
	v_cvt_pk_f16_f32 v151, v11, v19
	s_waitcnt vmcnt(12)
	v_cvt_pk_f16_f32 v173, v12, v20
	v_cvt_pk_f16_f32 v118, v13, v21
	v_cvt_pk_f16_f32 v126, v14, v22
	v_cvt_pk_f16_f32 v130, v15, v23
	v_accvgpr_write_b32 a28, v173
	v_accvgpr_write_b32 a60, v118
	v_accvgpr_write_b32 a92, v126
	v_accvgpr_write_b32 a124, v130
	v_accvgpr_write_b32 a156, v134
	v_accvgpr_write_b32 a183, v248
	v_accvgpr_write_b32 a184, v171
	v_accvgpr_write_b32 a185, v172
	v_accvgpr_write_b32 a186, v174
	v_accvgpr_write_b32 a187, v175
	s_waitcnt vmcnt(9)
	v_cvt_pk_f16_f32 v135, v24, v32
	v_cvt_pk_f16_f32 v139, v25, v33
	v_cvt_pk_f16_f32 v143, v26, v34
	v_cvt_pk_f16_f32 v152, v27, v35
	s_waitcnt vmcnt(8)
	v_cvt_pk_f16_f32 v182, v28, v36
	v_cvt_pk_f16_f32 v119, v29, v37
	v_cvt_pk_f16_f32 v127, v30, v38
	v_cvt_pk_f16_f32 v131, v31, v39
	v_accvgpr_write_b32 a29, v182
	v_accvgpr_write_b32 a61, v119
	v_accvgpr_write_b32 a93, v127
	v_accvgpr_write_b32 a125, v131
	v_accvgpr_write_b32 a157, v135
	v_accvgpr_write_b32 a188, v138
	v_accvgpr_write_b32 a189, v139
	v_accvgpr_write_b32 a212, v247
	v_accvgpr_write_b32 a213, v246
	v_accvgpr_write_b32 a214, v244
	s_waitcnt vmcnt(5)
	v_cvt_pk_f16_f32 v136, v40, v48
	v_cvt_pk_f16_f32 v140, v41, v49
	v_cvt_pk_f16_f32 v144, v42, v50
	v_cvt_pk_f16_f32 v153, v43, v51
	s_waitcnt vmcnt(4)
	v_cvt_pk_f16_f32 v184, v44, v52
	v_cvt_pk_f16_f32 v120, v45, v53
	v_cvt_pk_f16_f32 v128, v46, v54
	v_cvt_pk_f16_f32 v132, v47, v55
	v_accvgpr_write_b32 a30, v184
	v_accvgpr_write_b32 a62, v120
	v_accvgpr_write_b32 a94, v128
	v_accvgpr_write_b32 a126, v132
	v_accvgpr_write_b32 a158, v136
	v_accvgpr_write_b32 a190, v140
	v_accvgpr_write_b32 a215, v242
	v_accvgpr_write_b32 a216, v176
	v_accvgpr_write_b32 a217, v177
	s_waitcnt vmcnt(1)
	v_cvt_pk_f16_f32 v137, v56, v64
	v_cvt_pk_f16_f32 v141, v57, v65
	v_lshl_add_u64 v[64:65], s[12:13], 0, v[4:5]
	v_lshl_add_u64 v[0:1], v[64:65], 0, v[0:1]
	global_load_dwordx4 v[4:7], v[0:1], off offset:16
	global_load_dwordx4 v[8:11], v[0:1], off
	v_or_b32_e32 v0, 1, v200
	v_mov_b32_e32 v1, v201
	v_lshlrev_b64 v[0:1], 14, v[0:1]
	v_lshl_add_u64 v[0:1], v[64:65], 0, v[0:1]
	global_load_dwordx4 v[12:15], v[0:1], off offset:16
	global_load_dwordx4 v[16:19], v[0:1], off
	v_or_b32_e32 v0, 2, v200
	v_mov_b32_e32 v1, v201
	v_lshlrev_b64 v[0:1], 14, v[0:1]
	v_lshl_add_u64 v[0:1], v[64:65], 0, v[0:1]
	global_load_dwordx4 v[20:23], v[0:1], off offset:16
	global_load_dwordx4 v[24:27], v[0:1], off
	v_or_b32_e32 v0, 3, v200
	v_mov_b32_e32 v1, v201
	v_lshlrev_b64 v[0:1], 14, v[0:1]
	v_lshl_add_u64 v[0:1], v[64:65], 0, v[0:1]
	global_load_dwordx4 v[28:31], v[0:1], off offset:16
	global_load_dwordx4 v[32:35], v[0:1], off
	v_or_b32_e32 v0, 4, v200
	v_mov_b32_e32 v1, v201
	v_lshlrev_b64 v[0:1], 14, v[0:1]
	v_lshl_add_u64 v[0:1], v[64:65], 0, v[0:1]
	global_load_dwordx4 v[36:39], v[0:1], off offset:16
	global_load_dwordx4 v[40:43], v[0:1], off
	v_or_b32_e32 v0, 5, v200
	v_mov_b32_e32 v1, v201
	v_lshlrev_b64 v[0:1], 14, v[0:1]
	v_lshl_add_u64 v[0:1], v[64:65], 0, v[0:1]
	global_load_dwordx4 v[44:47], v[0:1], off offset:16
	global_load_dwordx4 v[48:51], v[0:1], off
	v_or_b32_e32 v0, 6, v200
	v_mov_b32_e32 v1, v201
	v_lshlrev_b64 v[0:1], 14, v[0:1]
	v_lshl_add_u64 v[0:1], v[64:65], 0, v[0:1]
	v_cvt_pk_f16_f32 v145, v58, v66
	v_cvt_pk_f16_f32 v154, v59, v67
	global_load_dwordx4 v[52:55], v[0:1], off offset:16
	global_load_dwordx4 v[56:59], v[0:1], off
	v_or_b32_e32 v0, 7, v200
	v_mov_b32_e32 v1, v201
	v_lshlrev_b64 v[0:1], 14, v[0:1]
	v_lshl_add_u64 v[0:1], v[64:65], 0, v[0:1]
	s_waitcnt vmcnt(14)
	v_cvt_pk_f16_f32 v209, v60, v68
	v_cvt_pk_f16_f32 v121, v61, v69
	v_cvt_pk_f16_f32 v129, v62, v70
	v_cvt_pk_f16_f32 v133, v63, v71
	global_load_dwordx4 v[60:63], v[0:1], off offset:16
	global_load_dwordx4 v[66:69], v[0:1], off
	v_or_b32_e32 v0, 32, v200
	v_mov_b32_e32 v1, v201
	v_lshlrev_b64 v[0:1], 14, v[0:1]
	v_lshl_add_u64 v[0:1], v[64:65], 0, v[0:1]
	v_readfirstlane_b32 s12, v186
	s_lshl_b32 s13, s19, 3
	v_or_b32_e32 v214, s13, v150
	v_ashrrev_i32_e32 v215, 31, v214
	v_accvgpr_write_b32 a31, v209
	v_accvgpr_write_b32 a63, v121
	v_accvgpr_write_b32 a95, v129
	v_accvgpr_write_b32 a127, v133
	v_accvgpr_write_b32 a159, v137
	v_accvgpr_write_b32 a191, v141
	v_accvgpr_write_b32 a218, v178
	v_accvgpr_write_b32 a219, v179
	v_accvgpr_write_b32 a220, v142
	v_accvgpr_write_b32 a221, v143
	v_accvgpr_write_b32 a222, v144
	v_accvgpr_write_b32 a223, v145
	v_accvgpr_write_b32 a244, v239
	v_accvgpr_write_b32 a245, v238
	v_accvgpr_write_b32 a246, v237
	v_accvgpr_write_b32 a247, v236
	v_accvgpr_write_b32 a248, v189
	v_accvgpr_write_b32 a249, v191
	v_accvgpr_write_b32 a250, v192
	v_accvgpr_write_b32 a251, v195
	v_accvgpr_write_b32 a252, v151
	v_accvgpr_write_b32 a253, v152
	v_accvgpr_write_b32 a254, v153
	v_accvgpr_write_b32 a255, v154
	s_waitcnt vmcnt(13)
	v_cvt_pk_f16_f32 v74, v4, v12
	s_waitcnt vmcnt(12)
	v_cvt_pk_f16_f32 v70, v8, v16
	v_cvt_pk_f16_f32 v78, v9, v17
	v_cvt_pk_f16_f32 v82, v5, v13
	v_cvt_pk_f16_f32 v86, v10, v18
	v_cvt_pk_f16_f32 v2, v6, v14
	v_cvt_pk_f16_f32 v8, v7, v15
	s_waitcnt vmcnt(9)
	v_cvt_pk_f16_f32 v75, v20, v28
	s_waitcnt vmcnt(8)
	v_cvt_pk_f16_f32 v71, v24, v32
	v_cvt_pk_f16_f32 v79, v25, v33
	v_cvt_pk_f16_f32 v83, v21, v29
	v_cvt_pk_f16_f32 v87, v26, v34
	v_cvt_pk_f16_f32 v3, v22, v30
	v_cvt_pk_f16_f32 v27, v27, v35
	v_cvt_pk_f16_f32 v26, v11, v19
	v_cvt_pk_f16_f32 v9, v23, v31
	s_waitcnt vmcnt(5)
	v_cvt_pk_f16_f32 v76, v36, v44
	s_waitcnt vmcnt(4)
	v_cvt_pk_f16_f32 v72, v40, v48
	v_cvt_pk_f16_f32 v80, v41, v49
	v_cvt_pk_f16_f32 v84, v37, v45
	v_cvt_pk_f16_f32 v88, v42, v50
	v_cvt_pk_f16_f32 v4, v38, v46
	v_cvt_pk_f16_f32 v28, v43, v51
	v_cvt_pk_f16_f32 v10, v39, v47
	s_waitcnt vmcnt(1)
	v_cvt_pk_f16_f32 v77, v52, v60
	s_waitcnt vmcnt(0)
	v_cvt_pk_f16_f32 v73, v56, v66
	v_cvt_pk_f16_f32 v81, v57, v67
	v_cvt_pk_f16_f32 v85, v53, v61
	v_cvt_pk_f16_f32 v89, v58, v68
	v_cvt_pk_f16_f32 v5, v54, v62
	v_cvt_pk_f16_f32 v29, v59, v69
	v_cvt_pk_f16_f32 v11, v55, v63
	ds_write_b128 v95, v[70:73]
	ds_write_b128 v95, v[78:81] offset:1024
	ds_write_b128 v95, v[86:89] offset:2048
	ds_write_b128 v95, v[26:29] offset:3072
	ds_write_b128 v95, v[74:77] offset:4096
	ds_write_b128 v95, v[82:85] offset:5120
	ds_write_b128 v95, v[2:5] offset:6144
	ds_write_b128 v95, v[8:11] offset:7168
	global_load_dwordx4 v[4:7], v[0:1], off offset:16
	global_load_dwordx4 v[12:15], v[0:1], off
	v_or_b32_e32 v0, 33, v200
	v_mov_b32_e32 v1, v201
	v_lshlrev_b64 v[0:1], 14, v[0:1]
	v_lshl_add_u64 v[0:1], v[64:65], 0, v[0:1]
	global_load_dwordx4 v[8:11], v[0:1], off offset:16
	global_load_dwordx4 v[16:19], v[0:1], off
	v_or_b32_e32 v0, 34, v200
	v_mov_b32_e32 v1, v201
	v_lshlrev_b64 v[0:1], 14, v[0:1]
	v_lshl_add_u64 v[0:1], v[64:65], 0, v[0:1]
	global_load_dwordx4 v[20:23], v[0:1], off offset:16
	global_load_dwordx4 v[32:35], v[0:1], off
	v_or_b32_e32 v0, 35, v200
	v_mov_b32_e32 v1, v201
	v_lshlrev_b64 v[0:1], 14, v[0:1]
	v_lshl_add_u64 v[0:1], v[64:65], 0, v[0:1]
	global_load_dwordx4 v[24:27], v[0:1], off offset:16
	global_load_dwordx4 v[40:43], v[0:1], off
	v_or_b32_e32 v0, 36, v200
	v_mov_b32_e32 v1, v201
	v_lshlrev_b64 v[0:1], 14, v[0:1]
	v_lshl_add_u64 v[0:1], v[64:65], 0, v[0:1]
	global_load_dwordx4 v[28:31], v[0:1], off offset:16
	global_load_dwordx4 v[44:47], v[0:1], off
	v_or_b32_e32 v0, 37, v200
	v_mov_b32_e32 v1, v201
	v_lshlrev_b64 v[0:1], 14, v[0:1]
	v_lshl_add_u64 v[0:1], v[64:65], 0, v[0:1]
	global_load_dwordx4 v[36:39], v[0:1], off offset:16
	global_load_dwordx4 v[48:51], v[0:1], off
	v_or_b32_e32 v0, 38, v200
	v_mov_b32_e32 v1, v201
	v_lshlrev_b64 v[0:1], 14, v[0:1]
	v_lshl_add_u64 v[0:1], v[64:65], 0, v[0:1]
	global_load_dwordx4 v[52:55], v[0:1], off offset:16
	global_load_dwordx4 v[56:59], v[0:1], off
	v_or_b32_e32 v0, 39, v200
	v_mov_b32_e32 v1, v201
	v_lshlrev_b64 v[0:1], 14, v[0:1]
	v_lshl_add_u64 v[0:1], v[64:65], 0, v[0:1]
	global_load_dwordx4 v[60:63], v[0:1], off offset:16
	global_load_dwordx4 v[66:69], v[0:1], off
	v_or_b32_e32 v0, s0, v193
	v_lshlrev_b32_e32 v94, 4, v0
	v_or_b32_e32 v0, 0x3c00, v94
	v_mov_b32_e32 v1, v201
	v_bfe_u32 v193, v193, 3, 1
	v_cmp_gt_u32_e64 s[0:1], 8, v220
	s_waitcnt vmcnt(13)
	v_cvt_pk_f16_f32 v74, v4, v8
	s_waitcnt vmcnt(12)
	v_cvt_pk_f16_f32 v70, v12, v16
	v_cvt_pk_f16_f32 v78, v13, v17
	v_cvt_pk_f16_f32 v2, v14, v18
	v_cvt_pk_f16_f32 v12, v7, v11
	v_cvt_pk_f16_f32 v82, v5, v9
	v_cvt_pk_f16_f32 v86, v6, v10
	s_waitcnt vmcnt(9)
	v_cvt_pk_f16_f32 v13, v23, v27
	s_waitcnt vmcnt(8)
	v_cvt_pk_f16_f32 v71, v32, v40
	v_cvt_pk_f16_f32 v3, v34, v42
	v_cvt_pk_f16_f32 v34, v15, v19
	v_cvt_pk_f16_f32 v75, v20, v24
	v_cvt_pk_f16_f32 v79, v33, v41
	v_cvt_pk_f16_f32 v83, v21, v25
	v_cvt_pk_f16_f32 v87, v22, v26
	v_cvt_pk_f16_f32 v35, v35, v43
	s_waitcnt vmcnt(5)
	v_cvt_pk_f16_f32 v14, v31, v39
	s_waitcnt vmcnt(4)
	v_cvt_pk_f16_f32 v72, v44, v48
	v_cvt_pk_f16_f32 v76, v28, v36
	v_cvt_pk_f16_f32 v80, v45, v49
	v_cvt_pk_f16_f32 v84, v29, v37
	v_cvt_pk_f16_f32 v4, v46, v50
	v_cvt_pk_f16_f32 v88, v30, v38
	v_cvt_pk_f16_f32 v36, v47, v51
	s_waitcnt vmcnt(1)
	v_cvt_pk_f16_f32 v15, v55, v63
	s_waitcnt vmcnt(0)
	v_cvt_pk_f16_f32 v73, v56, v66
	v_cvt_pk_f16_f32 v77, v52, v60
	v_cvt_pk_f16_f32 v81, v57, v67
	v_cvt_pk_f16_f32 v85, v53, v61
	v_cvt_pk_f16_f32 v5, v58, v68
	v_cvt_pk_f16_f32 v89, v54, v62
	v_cvt_pk_f16_f32 v37, v59, v69
	ds_write_b128 v95, v[70:73] offset:8192
	ds_write_b128 v95, v[78:81] offset:9216
	ds_write_b128 v95, v[2:5] offset:10240
	ds_write_b128 v95, v[34:37] offset:11264
	ds_write_b128 v95, v[74:77] offset:12288
	ds_write_b128 v95, v[82:85] offset:13312
	ds_write_b128 v95, v[86:89] offset:14336
	ds_write_b128 v0, v[12:15]
	v_or_b32_e32 v0, 64, v200
	v_lshlrev_b64 v[0:1], 14, v[0:1]
	v_lshl_add_u64 v[0:1], v[64:65], 0, v[0:1]
	global_load_dwordx4 v[4:7], v[0:1], off offset:16
	global_load_dwordx4 v[8:11], v[0:1], off
	v_or_b32_e32 v0, 0x41, v200
	v_mov_b32_e32 v1, v201
	v_lshlrev_b64 v[0:1], 14, v[0:1]
	v_lshl_add_u64 v[0:1], v[64:65], 0, v[0:1]
	global_load_dwordx4 v[12:15], v[0:1], off offset:16
	global_load_dwordx4 v[16:19], v[0:1], off
	v_or_b32_e32 v0, 0x42, v200
	v_mov_b32_e32 v1, v201
	v_lshlrev_b64 v[0:1], 14, v[0:1]
	v_lshl_add_u64 v[0:1], v[64:65], 0, v[0:1]
	global_load_dwordx4 v[20:23], v[0:1], off offset:16
	global_load_dwordx4 v[28:31], v[0:1], off
	v_or_b32_e32 v0, 0x43, v200
	v_mov_b32_e32 v1, v201
	v_lshlrev_b64 v[0:1], 14, v[0:1]
	v_lshl_add_u64 v[0:1], v[64:65], 0, v[0:1]
	global_load_dwordx4 v[24:27], v[0:1], off offset:16
	global_load_dwordx4 v[32:35], v[0:1], off
	v_or_b32_e32 v0, 0x44, v200
	v_mov_b32_e32 v1, v201
	v_lshlrev_b64 v[0:1], 14, v[0:1]
	v_lshl_add_u64 v[0:1], v[64:65], 0, v[0:1]
	global_load_dwordx4 v[36:39], v[0:1], off offset:16
	global_load_dwordx4 v[40:43], v[0:1], off
	v_or_b32_e32 v0, 0x45, v200
	v_mov_b32_e32 v1, v201
	v_lshlrev_b64 v[0:1], 14, v[0:1]
	v_lshl_add_u64 v[0:1], v[64:65], 0, v[0:1]
	global_load_dwordx4 v[44:47], v[0:1], off offset:16
	global_load_dwordx4 v[48:51], v[0:1], off
	v_or_b32_e32 v0, 0x46, v200
	v_mov_b32_e32 v1, v201
	v_lshlrev_b64 v[0:1], 14, v[0:1]
	v_lshl_add_u64 v[0:1], v[64:65], 0, v[0:1]
	global_load_dwordx4 v[52:55], v[0:1], off offset:16
	global_load_dwordx4 v[56:59], v[0:1], off
	v_or_b32_e32 v0, 0x47, v200
	v_mov_b32_e32 v1, v201
	v_lshlrev_b64 v[0:1], 14, v[0:1]
	v_lshl_add_u64 v[0:1], v[64:65], 0, v[0:1]
	global_load_dwordx4 v[60:63], v[0:1], off offset:16
	global_load_dwordx4 v[66:69], v[0:1], off
	v_or_b32_e32 v0, 0x60, v200
	v_mov_b32_e32 v1, v201
	v_lshlrev_b64 v[0:1], 14, v[0:1]
	v_lshl_add_u64 v[0:1], v[64:65], 0, v[0:1]
	s_waitcnt vmcnt(13)
	v_cvt_pk_f16_f32 v74, v4, v12
	s_waitcnt vmcnt(12)
	v_cvt_pk_f16_f32 v70, v8, v16
	v_cvt_pk_f16_f32 v78, v9, v17
	v_cvt_pk_f16_f32 v82, v5, v13
	v_cvt_pk_f16_f32 v2, v10, v18
	v_cvt_pk_f16_f32 v86, v6, v14
	v_cvt_pk_f16_f32 v8, v7, v15
	s_waitcnt vmcnt(9)
	v_cvt_pk_f16_f32 v75, v20, v24
	s_waitcnt vmcnt(8)
	v_cvt_pk_f16_f32 v71, v28, v32
	v_cvt_pk_f16_f32 v79, v29, v33
	v_cvt_pk_f16_f32 v83, v21, v25
	v_cvt_pk_f16_f32 v3, v30, v34
	v_cvt_pk_f16_f32 v87, v22, v26
	v_cvt_pk_f16_f32 v31, v31, v35
	v_cvt_pk_f16_f32 v30, v11, v19
	v_cvt_pk_f16_f32 v9, v23, v27
	s_waitcnt vmcnt(5)
	v_cvt_pk_f16_f32 v76, v36, v44
	s_waitcnt vmcnt(4)
	v_cvt_pk_f16_f32 v72, v40, v48
	v_cvt_pk_f16_f32 v80, v41, v49
	v_cvt_pk_f16_f32 v84, v37, v45
	v_cvt_pk_f16_f32 v4, v42, v50
	v_cvt_pk_f16_f32 v88, v38, v46
	v_cvt_pk_f16_f32 v32, v43, v51
	v_cvt_pk_f16_f32 v10, v39, v47
	s_waitcnt vmcnt(1)
	v_cvt_pk_f16_f32 v77, v52, v60
	s_waitcnt vmcnt(0)
	v_cvt_pk_f16_f32 v73, v56, v66
	v_cvt_pk_f16_f32 v81, v57, v67
	v_cvt_pk_f16_f32 v85, v53, v61
	v_cvt_pk_f16_f32 v5, v58, v68
	v_cvt_pk_f16_f32 v89, v54, v62
	v_cvt_pk_f16_f32 v33, v59, v69
	v_cvt_pk_f16_f32 v11, v55, v63
	ds_write_b128 v95, v[70:73] offset:16384
	ds_write_b128 v95, v[78:81] offset:17408
	ds_write_b128 v95, v[2:5] offset:18432
	ds_write_b128 v95, v[30:33] offset:19456
	ds_write_b128 v95, v[74:77] offset:20480
	ds_write_b128 v95, v[82:85] offset:21504
	ds_write_b128 v95, v[86:89] offset:22528
	ds_write_b128 v95, v[8:11] offset:23552
	global_load_dwordx4 v[8:11], v[0:1], off offset:16
	global_load_dwordx4 v[40:43], v[0:1], off
	v_or_b32_e32 v0, 0x61, v200
	v_mov_b32_e32 v1, v201
	v_lshlrev_b64 v[0:1], 14, v[0:1]
	v_lshl_add_u64 v[0:1], v[64:65], 0, v[0:1]
	global_load_dwordx4 v[16:19], v[0:1], off offset:16
	global_load_dwordx4 v[48:51], v[0:1], off
	v_or_b32_e32 v0, 0x62, v200
	v_mov_b32_e32 v1, v201
	v_lshlrev_b64 v[0:1], 14, v[0:1]
	v_lshl_add_u64 v[0:1], v[64:65], 0, v[0:1]
	global_load_dwordx4 v[30:33], v[0:1], off offset:16
	global_load_dwordx4 v[56:59], v[0:1], off
	v_or_b32_e32 v0, 0x63, v200
	v_mov_b32_e32 v1, v201
	v_lshlrev_b64 v[0:1], 14, v[0:1]
	v_lshl_add_u64 v[0:1], v[64:65], 0, v[0:1]
	global_load_dwordx4 v[34:37], v[0:1], off offset:16
	global_load_dwordx4 v[60:63], v[0:1], off
	v_or_b32_e32 v0, 0x64, v200
	v_mov_b32_e32 v1, v201
	v_lshlrev_b64 v[0:1], 14, v[0:1]
	v_lshl_add_u64 v[0:1], v[64:65], 0, v[0:1]
	global_load_dwordx4 v[44:47], v[0:1], off offset:16
	global_load_dwordx4 v[72:75], v[0:1], off
	v_or_b32_e32 v0, 0x65, v200
	v_mov_b32_e32 v1, v201
	v_lshlrev_b64 v[0:1], 14, v[0:1]
	v_lshl_add_u64 v[0:1], v[64:65], 0, v[0:1]
	global_load_dwordx4 v[52:55], v[0:1], off offset:16
	global_load_dwordx4 v[80:83], v[0:1], off
	v_or_b32_e32 v0, 0x66, v200
	v_mov_b32_e32 v1, v201
	v_lshlrev_b64 v[0:1], 14, v[0:1]
	v_lshl_add_u64 v[0:1], v[64:65], 0, v[0:1]
	v_or_b32_e32 v200, 0x67, v200
	global_load_dwordx4 v[68:71], v[0:1], off offset:16
	global_load_dwordx4 v[84:87], v[0:1], off
	v_lshlrev_b64 v[0:1], 14, v[200:201]
	v_lshl_add_u64 v[0:1], v[64:65], 0, v[0:1]
	global_load_dwordx4 v[76:79], v[0:1], off offset:16
	s_nop 0
	global_load_dwordx4 v[0:3], v[0:1], off
	v_lshlrev_b32_e32 v200, 5, v109
	s_waitcnt vmcnt(13)
	v_cvt_pk_f16_f32 v4, v8, v16
	s_waitcnt vmcnt(12)
	v_cvt_pk_f16_f32 v64, v40, v48
	v_cvt_pk_f16_f32 v20, v41, v49
	v_cvt_pk_f16_f32 v12, v9, v17
	v_cvt_pk_f16_f32 v28, v42, v50
	v_cvt_pk_f16_f32 v24, v10, v18
	v_cvt_pk_f16_f32 v38, v43, v51
	s_waitcnt vmcnt(9)
	v_cvt_pk_f16_f32 v5, v30, v34
	s_waitcnt vmcnt(8)
	v_cvt_pk_f16_f32 v65, v56, v60
	v_cvt_pk_f16_f32 v13, v31, v35
	v_cvt_pk_f16_f32 v25, v32, v36
	v_cvt_pk_f16_f32 v33, v33, v37
	v_cvt_pk_f16_f32 v32, v11, v19
	v_cvt_pk_f16_f32 v21, v57, v61
	v_cvt_pk_f16_f32 v29, v58, v62
	v_cvt_pk_f16_f32 v39, v59, v63
	s_waitcnt vmcnt(5)
	v_cvt_pk_f16_f32 v26, v46, v54
	v_add_u32_e32 v54, s2, v208
	s_waitcnt vmcnt(4)
	v_cvt_pk_f16_f32 v66, v72, v80
	v_cvt_pk_f16_f32 v34, v47, v55
	v_ashrrev_i32_e32 v55, 31, v54
	v_cvt_pk_f16_f32 v6, v44, v52
	v_cvt_pk_f16_f32 v22, v73, v81
	v_cvt_pk_f16_f32 v14, v45, v53
	v_cvt_pk_f16_f32 v30, v74, v82
	s_waitcnt vmcnt(1)
	v_cvt_pk_f16_f32 v35, v71, v79
	s_waitcnt vmcnt(0)
	v_cvt_pk_f16_f32 v67, v84, v0
	v_or_b32_e32 v0, 0x7c00, v94
	v_cvt_pk_f16_f32 v7, v68, v76
	v_cvt_pk_f16_f32 v23, v85, v1
	v_cvt_pk_f16_f32 v15, v69, v77
	v_cvt_pk_f16_f32 v31, v86, v2
	v_cvt_pk_f16_f32 v27, v70, v78
	v_cvt_pk_f16_f32 v41, v87, v3
	v_cvt_pk_f16_f32 v40, v75, v83
	ds_write_b128 v95, v[64:67] offset:24576
	ds_write_b128 v95, v[20:23] offset:25600
	ds_write_b128 v95, v[28:31] offset:26624
	ds_write_b128 v95, v[38:41] offset:27648
	ds_write_b128 v95, v[4:7] offset:28672
	ds_write_b128 v95, v[12:15] offset:29696
	ds_write_b128 v95, v[24:27] offset:30720
	ds_write_b128 v0, v[32:35]
	v_lshl_add_u64 v[0:1], v[54:55], 2, s[4:5]
	global_load_dword v185, v[0:1], off
	v_add_u32_e32 v0, 0x400, v54
	v_ashrrev_i32_e32 v1, 31, v0
	v_lshl_add_u64 v[0:1], v[0:1], 2, s[4:5]
	global_load_dword v186, v[0:1], off
	v_add_u32_e32 v0, 0x800, v54
	v_ashrrev_i32_e32 v1, 31, v0
	v_lshl_add_u64 v[0:1], v[0:1], 2, s[4:5]
	global_load_dword v187, v[0:1], off
	v_add_u32_e32 v0, 0xc00, v54
	v_ashrrev_i32_e32 v1, 31, v0
	v_lshl_add_u64 v[0:1], v[0:1], 2, s[4:5]
	global_load_dword v188, v[0:1], off
	v_lshlrev_b64 v[0:1], 20, v[214:215]
	v_lshl_add_u64 v[0:1], s[16:17], 0, v[0:1]
	v_lshl_add_u64 v[0:1], s[14:15], 2, v[0:1]
	v_lshl_add_u64 v[210:211], v[0:1], 0, v[200:201]
	global_load_dwordx4 v[4:7], v[210:211], off offset:256
	global_load_dwordx4 v[8:11], v[210:211], off offset:272
	global_load_dwordx4 v[14:17], v[210:211], off offset:384
	global_load_dwordx4 v[18:21], v[210:211], off offset:400
	v_lshlrev_b32_e32 v0, 4, v198
	s_waitcnt lgkmcnt(0)
	s_barrier
	ds_read_b128 v[96:99], v0 offset:23552
	ds_read_b128 v[92:95], v0 offset:22528
	ds_read_b128 v[88:91], v0 offset:21504
	ds_read_b128 v[60:63], v0 offset:20480
	ds_read_b128 v[64:67], v0 offset:19456
	ds_read_b128 v[68:71], v0 offset:18432
	ds_read_b128 v[72:75], v0 offset:17408
	ds_read_b128 v[76:79], v0 offset:16384
	v_mov_b64_e32 v[44:45], s[26:27]
	v_mov_b64_e32 v[40:41], s[26:27]
	v_mov_b64_e32 v[22:23], s[24:25]
	v_mov_b64_e32 v[28:29], s[26:27]
	v_mov_b64_e32 v[32:33], s[26:27]
	v_mov_b64_e32 v[36:37], s[26:27]
	v_mov_b64_e32 v[42:43], s[24:25]
	v_mov_b64_e32 v[38:39], s[24:25]
	v_mov_b64_e32 v[24:25], s[26:27]
	v_mov_b64_e32 v[26:27], s[24:25]
	v_mov_b64_e32 v[30:31], s[24:25]
	v_mov_b64_e32 v[34:35], s[24:25]
	s_or_b32 s4, s3, s13
	s_ashr_i32 s5, s4, 31
	s_lshl_b64 s[4:5], s[4:5], 20
	s_add_u32 s4, s16, s4
	s_addc_u32 s5, s17, s5
	s_cmp_lg_u32 s12, 0
	v_mov_b32_e32 v200, v201
	s_waitcnt vmcnt(3)
	v_cvt_pk_f16_f32 v101, v6, v7
	s_waitcnt vmcnt(2)
	v_cvt_pk_f16_f32 v103, v10, v11
	v_cvt_pk_f16_f32 v102, v8, v9
	v_cvt_pk_f16_f32 v100, v4, v5
	ds_read_b128 v[80:83], v0 offset:31744
	ds_read_b128 v[84:87], v0 offset:30720
	ds_read_b128 v[56:59], v0 offset:29696
	ds_read_b128 v[50:53], v0 offset:28672
	ds_read_b128 v[46:49], v0 offset:27648
	ds_read_b128 v[8:11], v0 offset:26624
	ds_read_b128 v[4:7], v0 offset:25600
	ds_read_b128 v[0:3], v0 offset:24576
	s_waitcnt vmcnt(0)
	v_cvt_pk_f16_f32 v107, v20, v21
	v_cvt_pk_f16_f32 v106, v18, v19
	v_cvt_pk_f16_f32 v105, v16, v17
	v_cvt_pk_f16_f32 v104, v14, v15
	v_mov_b64_e32 v[14:15], s[24:25]
	v_mov_b64_e32 v[18:19], s[24:25]
	v_mov_b64_e32 v[16:17], s[26:27]
	v_mov_b64_e32 v[20:21], s[26:27]
	s_waitcnt lgkmcnt(8)
	s_nop 1
	v_mfma_f32_16x16x32_f16 v[42:45], v[76:79], v[100:103], v[42:45]
	v_mfma_f32_16x16x32_f16 v[38:41], v[72:75], v[100:103], v[38:41]
	v_mfma_f32_16x16x32_f16 v[14:17], v[68:71], v[100:103], v[14:17]
	v_mfma_f32_16x16x32_f16 v[18:21], v[64:67], v[100:103], v[18:21]
	v_mfma_f32_16x16x32_f16 v[22:25], v[60:63], v[100:103], v[22:25]
	v_mfma_f32_16x16x32_f16 v[26:29], v[88:91], v[100:103], v[26:29]
	v_mfma_f32_16x16x32_f16 v[30:33], v[92:95], v[100:103], v[30:33]
	v_mfma_f32_16x16x32_f16 v[34:37], v[96:99], v[100:103], v[34:37]
	v_lshlrev_b32_e32 v103, 4, v150
	s_waitcnt lgkmcnt(0)
	s_nop 1
	v_mfma_f32_16x16x32_f16 v[42:45], v[0:3], v[104:107], v[42:45]
	v_mfma_f32_16x16x32_f16 v[38:41], v[4:7], v[104:107], v[38:41]
	v_mfma_f32_16x16x32_f16 v[14:17], v[8:11], v[104:107], v[14:17]
	v_mfma_f32_16x16x32_f16 v[18:21], v[46:49], v[104:107], v[18:21]
	v_mfma_f32_16x16x32_f16 v[22:25], v[50:53], v[104:107], v[22:25]
	v_mfma_f32_16x16x32_f16 v[26:29], v[56:59], v[104:107], v[26:29]
	v_mfma_f32_16x16x32_f16 v[30:33], v[84:87], v[104:107], v[30:33]
	v_mfma_f32_16x16x32_f16 v[34:37], v[80:83], v[104:107], v[34:37]
	v_lshlrev_b32_e32 v0, 11, v193
	v_mov_b32_e32 v1, v201
	s_nop 15
	s_nop 7
	v_lshl_add_u64 v[0:1], v[210:211], 0, v[0:1]
	v_cndmask_b32_e64 v6, 0, v42, s[0:1]
	v_cndmask_b32_e64 v7, 0, v43, s[0:1]
	v_cndmask_b32_e64 v8, 0, v44, s[0:1]
	v_cndmask_b32_e64 v9, 0, v45, s[0:1]
	v_cndmask_b32_e64 v10, 0, v38, s[0:1]
	v_cndmask_b32_e64 v11, 0, v39, s[0:1]
	v_cndmask_b32_e64 v12, 0, v40, s[0:1]
	v_cndmask_b32_e64 v13, 0, v41, s[0:1]
	global_load_dwordx4 v[50:53], v[0:1], off offset:16
	global_load_dwordx4 v[46:49], v[0:1], off
	global_load_dwordx4 v[42:45], v[0:1], off offset:144
	global_load_dwordx4 v[38:41], v[0:1], off offset:128
	v_lshl_add_u32 v2, v220, 4, s14
	v_lshl_or_b32 v55, v207, 1, v2
	v_or_b32_e32 v2, s13, v220
	v_ashrrev_i32_e32 v3, 31, v2
	v_lshlrev_b32_e32 v0, 7, v109
	v_mov_b32_e32 v109, v201
	v_lshlrev_b64 v[2:3], 21, v[2:3]
	v_or3_b32 v104, v0, v103, s21
	v_lshl_add_u64 v[0:1], s[4:5], 0, v[108:109]
	s_cselect_b64 s[4:5], -1, 0
	v_lshl_add_u64 v[2:3], s[6:7], 0, v[2:3]
	s_ashr_i32 s3, s2, 31
	v_lshl_add_u64 v[2:3], s[2:3], 2, v[2:3]
	v_lshlrev_b32_e32 v4, 2, v208
	v_mov_b32_e32 v5, v201
	v_lshl_add_u64 v[96:97], v[2:3], 0, v[4:5]
	v_lshl_add_u32 v2, v214, 10, v54
	v_ashrrev_i32_e32 v3, 31, v2
	v_lshl_add_u64 v[2:3], v[2:3], 2, s[6:7]
	s_mov_b64 s[2:3], 0x8000000
	v_lshl_add_u64 v[98:99], v[2:3], 0, s[2:3]
	s_mov_b64 s[2:3], 0x8040000
	v_lshl_add_u64 v[100:101], v[2:3], 0, s[2:3]
	s_lshl_b32 s2, s19, 14
	s_lshl_b32 s3, s18, 9
	s_add_i32 s2, s2, s3
	v_mbcnt_lo_u32_b32 v2, -1, 0
	v_add_u32_e32 v106, s2, v55
	v_mbcnt_hi_u32_b32 v2, -1, v2
	v_mov_b64_e32 v[54:55], v[200:201]
	v_mov_b64_e32 v[58:59], v[200:201]
	v_cndmask_b32_e64 v14, 0, v14, s[0:1]
	v_cndmask_b32_e64 v15, 0, v15, s[0:1]
	v_cndmask_b32_e64 v16, 0, v16, s[0:1]
	v_cndmask_b32_e64 v17, 0, v17, s[0:1]
	v_cndmask_b32_e64 v18, 0, v18, s[0:1]
	v_cndmask_b32_e64 v19, 0, v19, s[0:1]
	v_cndmask_b32_e64 v20, 0, v20, s[0:1]
	v_cndmask_b32_e64 v21, 0, v21, s[0:1]
	v_cndmask_b32_e64 v22, 0, v22, s[0:1]
	v_cndmask_b32_e64 v23, 0, v23, s[0:1]
	v_cndmask_b32_e64 v24, 0, v24, s[0:1]
	v_cndmask_b32_e64 v25, 0, v25, s[0:1]
	v_cndmask_b32_e64 v26, 0, v26, s[0:1]
	v_cndmask_b32_e64 v27, 0, v27, s[0:1]
	v_cndmask_b32_e64 v28, 0, v28, s[0:1]
	v_cndmask_b32_e64 v29, 0, v29, s[0:1]
	v_cndmask_b32_e64 v30, 0, v30, s[0:1]
	v_cndmask_b32_e64 v31, 0, v31, s[0:1]
	v_cndmask_b32_e64 v32, 0, v32, s[0:1]
	v_cndmask_b32_e64 v33, 0, v33, s[0:1]
	v_cndmask_b32_e64 v34, 0, v34, s[0:1]
	v_cndmask_b32_e64 v35, 0, v35, s[0:1]
	v_cndmask_b32_e64 v36, 0, v36, s[0:1]
	v_cndmask_b32_e64 v37, 0, v37, s[0:1]
	v_lshlrev_b32_e32 v105, 9, v207
	s_mov_b64 s[6:7], 0
	s_mov_b32 s18, 0x40004000
	v_lshl_or_b32 v107, v2, 2, 32
	v_mov_b32_e32 v108, 0
	v_mov_b64_e32 v[56:57], v[202:203]
	v_mov_b64_e32 v[60:61], v[202:203]
	s_mov_b32 s24, 0
	v_lshl_add_u32 v166, s19, 14, v104
	v_mov_b32_e32 v177, 0
	s_mov_b32 s37, 0x4038aa3b
	s_mov_b32 s38, 0xbfb8aa3b
	s_waitcnt vmcnt(0)
	v_mul_f32_e32 v185, 0xbfb8aa3b, v185
	v_mul_f32_e32 v186, 0xbfb8aa3b, v186
	v_mul_f32_e32 v187, 0x4038aa3b, v187
	v_mul_f32_e32 v188, 0xbfb8aa3b, v188
	v_cvt_pk_f16_f32 v180, v46, v47
	v_cvt_pk_f16_f32 v181, v48, v49
	v_cvt_pk_f16_f32 v182, v50, v51
	v_cvt_pk_f16_f32 v183, v52, v53
	v_cvt_pk_f16_f32 v218, v38, v39
	v_cvt_pk_f16_f32 v219, v40, v41
	v_cvt_pk_f16_f32 v220, v42, v43
	v_cvt_pk_f16_f32 v221, v44, v45
	s_mov_b32 s25, 1
	v_bitop3_b32 v2, s25, v193, 1 bitop3:0x6c
	v_add_u32_e32 v2, s25, v2
	v_min_i32_e32 v2, 0x1ff, v2
	s_and_b32 s12, s25, 1
	v_lshlrev_b32_e32 v200, 11, v2
	v_lshl_add_u64 v[2:3], v[210:211], 0, v[200:201]
	s_lshl_b32 s14, s12, 8
	v_lshl_add_u64 v[4:5], v[2:3], 0, s[14:15]
	global_load_dwordx4 v[46:49], v[4:5], off
	global_load_dwordx4 v[50:53], v[4:5], off offset:16
	global_load_dwordx4 v[38:41], v[4:5], off offset:128
	global_load_dwordx4 v[42:45], v[4:5], off offset:144
.Lstep_top:
	s_and_b32 s16, s24, 1
	v_cmp_eq_u32_e64 s[2:3], s16, v193
	s_xor_b32 s33, s16, 1
	s_lshl_b32 s28, s33, 17
	s_add_i32 s25, s24, 1
	s_add_i32 s27, s24, 2
	s_mov_b32 s17, 0
	s_lshl_b32 s12, s16, 10
	v_or_b32_e32 v222, s12, v198
	v_lshlrev_b32_e32 v222, 4, v222
	ds_read_b128 v[130:133], v222
	ds_read_b128 v[126:129], v222 offset:1024
	ds_read_b128 v[122:125], v222 offset:2048
	ds_read_b128 v[118:121], v222 offset:3072
	ds_read_b128 v[114:117], v222 offset:4096
	ds_read_b128 v[110:113], v222 offset:5120
	ds_read_b128 v[194:197], v222 offset:6144
	ds_read_b128 v[202:205], v222 offset:7168
	ds_read_b128 v[162:165], v222 offset:8192
	ds_read_b128 v[158:161], v222 offset:9216
	ds_read_b128 v[154:157], v222 offset:10240
	ds_read_b128 v[150:153], v222 offset:11264
	ds_read_b128 v[146:149], v222 offset:12288
	ds_read_b128 v[142:145], v222 offset:13312
	ds_read_b128 v[138:141], v222 offset:14336
	ds_read_b128 v[134:137], v222 offset:15360
	s_cmp_eq_u32 s24, 0
	s_cbranch_scc1 .Lpoll_issued
	buffer_load_dwordx4 v[62:65], v166, s[8:11], s28 offen sc1
	buffer_load_dwordx4 v[66:69], v166, s[8:11], s28 offen offset:512 sc1
	buffer_load_dwordx4 v[70:73], v166, s[8:11], s28 offen offset:1024 sc1
	buffer_load_dwordx4 v[74:77], v166, s[8:11], s28 offen offset:1536 sc1
	buffer_load_dwordx4 v[78:81], v166, s[8:11], s28 offen offset:2048 sc1
	buffer_load_dwordx4 v[82:85], v166, s[8:11], s28 offen offset:2560 sc1
	buffer_load_dwordx4 v[86:89], v166, s[8:11], s28 offen offset:3072 sc1
	buffer_load_dwordx4 v[90:93], v166, s[8:11], s28 offen offset:3584 sc1
.Lpoll_issued:
	s_andn2_b64 exec, exec, s[2:3]
	v_mov_b64_e32 v[6:7], 0
	v_mov_b64_e32 v[8:9], 0
	v_mov_b64_e32 v[10:11], 0
	v_mov_b64_e32 v[12:13], 0
	v_mov_b64_e32 v[14:15], 0
	v_mov_b64_e32 v[16:17], 0
	v_mov_b64_e32 v[18:19], 0
	v_mov_b64_e32 v[20:21], 0
	v_mov_b64_e32 v[22:23], 0
	v_mov_b64_e32 v[24:25], 0
	v_mov_b64_e32 v[26:27], 0
	v_mov_b64_e32 v[28:29], 0
	v_mov_b64_e32 v[30:31], 0
	v_mov_b64_e32 v[32:33], 0
	v_mov_b64_e32 v[34:35], 0
	v_mov_b64_e32 v[36:37], 0
	s_mov_b64 exec, -1
	s_waitcnt lgkmcnt(8)
	v_mfma_f32_16x16x32_f16 v[6:9], v[130:133], v[180:183], v[6:9]
	s_add_i32 s12, s24, -1
	s_bfe_i32 s13, s12, 0x10001
	s_and_b32 s30, s13, 0x40004000
	v_mfma_f32_16x16x32_f16 v[10:13], v[126:129], v[180:183], v[10:13]
	v_mov_b32_e32 v3, 0xbfffbfff
	v_cndmask_b32_e64 v167, 0, v3, s[2:3]
	s_lshl_b32 s34, s24, 13
	v_mfma_f32_16x16x32_f16 v[14:17], v[122:125], v[180:183], v[14:17]
	s_and_b32 s34, s34, 0x4000
	s_lshl_b32 s14, s24, 10
	v_lshl_add_u64 v[178:179], s[14:15], 2, v[96:97]
	v_mfma_f32_16x16x32_f16 v[18:21], v[118:121], v[180:183], v[18:21]
	v_bitop3_b32 v2, s27, v193, 1 bitop3:0x6c
	v_add_u32_e32 v2, s27, v2
	v_min_i32_e32 v2, 0x1ff, v2
	v_mfma_f32_16x16x32_f16 v[22:25], v[114:117], v[180:183], v[22:25]
	s_and_b32 s12, s27, 1
	v_lshlrev_b32_e32 v200, 11, v2
	v_lshl_add_u64 v[2:3], v[210:211], 0, v[200:201]
	v_mfma_f32_16x16x32_f16 v[26:29], v[110:113], v[180:183], v[26:29]
	s_lshl_b32 s14, s12, 8
	v_lshl_add_u64 v[4:5], v[2:3], 0, s[14:15]
	s_lshl_b32 s35, s16, 14
	v_mfma_f32_16x16x32_f16 v[30:33], v[194:197], v[180:183], v[30:33]
	s_bitset1_b32 s35, 17
	s_add_i32 s26, s35, s21
	v_lshlrev_b32_e32 v2, 4, v217
	v_mfma_f32_16x16x32_f16 v[34:37], v[202:205], v[180:183], v[34:37]
	v_add3_u32 v174, s26, v2, v103
	s_lshl_b32 s12, s20, 4
	s_add_i32 s12, s12, s35
	s_waitcnt lgkmcnt(0)
	v_mfma_f32_16x16x32_f16 v[6:9], v[162:165], v[218:221], v[6:9]
	v_add3_u32 v175, s12, v105, v103
	v_lshl_add_u32 v176, s16, 17, v106
	v_mfma_f32_16x16x32_f16 v[10:13], v[158:161], v[218:221], v[10:13]
	s_and_b32 s31, s24, 15
	s_and_b32 s12, s24, 0x1f0
	v_mfma_f32_16x16x32_f16 v[14:17], v[154:157], v[218:221], v[14:17]
	s_add_i32 s12, s23, s12
	s_min_i32 s12, s12, 0x1ff
	s_waitcnt vmcnt(7)
	v_mfma_f32_16x16x32_f16 v[18:21], v[150:153], v[218:221], v[18:21]
	v_bitop3_b32 v168, v62, v63, s30 bitop3:0x7e
	v_bitop3_b32 v169, v64, v65, s30 bitop3:0x7e
	v_mfma_f32_16x16x32_f16 v[22:25], v[146:149], v[218:221], v[22:25]
	v_bitop3_b32 v168, v168, v169, s18 bitop3:0xa8
	v_cmp_ne_u32_e32 vcc, 0, v168
	v_mfma_f32_16x16x32_f16 v[26:29], v[142:145], v[218:221], v[26:29]
	v_and_b32_e32 v62, v62, v167
	v_and_b32_e32 v63, v63, v167
	v_mfma_f32_16x16x32_f16 v[30:33], v[138:141], v[218:221], v[30:33]
	v_and_b32_e32 v64, v64, v167
	v_and_b32_e32 v65, v65, v167
	v_mfma_f32_16x16x32_f16 v[34:37], v[134:137], v[218:221], v[34:37]
	s_ashr_i32 s13, s12, 31
	s_lshl_b64 s[12:13], s[12:13], 11
	v_lshl_add_u64 v[172:173], v[0:1], 0, s[12:13]
	s_cmp_eq_u32 s24, 0
	s_cbranch_scc1 .Lfirst_step
	s_cbranch_vccnz .Lrestart0
.Lfast0:
	v_mfma_f32_16x16x32_f16 v[6:9], a[0:3], v[62:65], v[6:9]
	v_cvt_pk_f16_f32 v180, v46, v47
	v_cvt_pk_f16_f32 v181, v48, v49
	v_mfma_f32_16x16x32_f16 v[10:13], a[32:35], v[62:65], v[10:13]
	v_cvt_pk_f16_f32 v182, v50, v51
	v_cvt_pk_f16_f32 v183, v52, v53
	v_mfma_f32_16x16x32_f16 v[14:17], a[64:67], v[62:65], v[14:17]
	v_cvt_pk_f16_f32 v218, v38, v39
	v_cvt_pk_f16_f32 v219, v40, v41
	s_waitcnt vmcnt(6)
	v_mfma_f32_16x16x32_f16 v[18:21], a[96:99], v[62:65], v[18:21]
	v_bitop3_b32 v168, v66, v67, s30 bitop3:0x7e
	v_bitop3_b32 v169, v68, v69, s30 bitop3:0x7e
	v_mfma_f32_16x16x32_f16 v[22:25], a[128:131], v[62:65], v[22:25]
	v_bitop3_b32 v168, v168, v169, s18 bitop3:0xa8
	v_cmp_ne_u32_e32 vcc, 0, v168
	v_mfma_f32_16x16x32_f16 v[26:29], a[160:163], v[62:65], v[26:29]
	v_and_b32_e32 v66, v66, v167
	v_and_b32_e32 v67, v67, v167
	v_mfma_f32_16x16x32_f16 v[30:33], a[192:195], v[62:65], v[30:33]
	v_and_b32_e32 v68, v68, v167
	v_and_b32_e32 v69, v69, v167
	v_mfma_f32_16x16x32_f16 v[34:37], a[224:227], v[62:65], v[34:37]
	v_cvt_pk_f16_f32 v220, v42, v43
	v_cvt_pk_f16_f32 v221, v44, v45
	s_cbranch_vccnz .Lrestart1

.Lall_chunks_done:
	s_and_saveexec_b64 s[12:13], s[2:3]
	ds_write_b128 v174, v[6:9]
	ds_write_b128 v174, v[10:13] offset:512
	ds_write_b128 v174, v[14:17] offset:1024
	ds_write_b128 v174, v[18:21] offset:1536
	ds_write_b128 v174, v[22:25] offset:2048
	ds_write_b128 v174, v[26:29] offset:2560
	ds_write_b128 v174, v[30:33] offset:3072
	ds_write_b128 v174, v[34:37] offset:3584
	s_or_b64 exec, exec, s[12:13]
	global_load_dwordx4 v[46:49], v[4:5], off
	global_load_dwordx4 v[50:53], v[4:5], off offset:16
	global_load_dwordx4 v[38:41], v[4:5], off offset:128
	global_load_dwordx4 v[42:45], v[4:5], off offset:144
	s_cmp_lg_u32 s31, 0
	s_cbranch_scc1 .Lno_warm
	global_load_dwordx4 v[54:57], v[172:173], off
	global_load_dwordx4 v[58:61], v[172:173], off offset:1024
.Lno_warm:
	s_waitcnt lgkmcnt(0)
	s_barrier
	ds_read_b128 v[2:5], v175
	ds_read_b128 v[110:113], v175 offset:4096
	ds_read_b128 v[114:117], v175 offset:8192
	ds_read_b128 v[118:121], v175 offset:12288
	s_waitcnt lgkmcnt(0)
	v_pk_add_f32 v[4:5], v[4:5], v[112:113]
	v_pk_add_f32 v[2:3], v[2:3], v[110:111]
	v_pk_add_f32 v[4:5], v[4:5], v[116:117]
	v_pk_add_f32 v[2:3], v[2:3], v[114:115]
	v_pk_add_f32 v[4:5], v[4:5], v[120:121]
	v_pk_add_f32 v[2:3], v[2:3], v[118:119]
	v_fma_f32 v4, v4, s37, v187
	v_fma_f32 v2, v2, s38, v185
	v_exp_f32_e32 v4, v4
	v_fma_f32 v3, v3, s38, v186
	v_exp_f32_e32 v2, v2
	v_fma_f32 v5, v5, s38, v188
	v_exp_f32_e32 v3, v3
	v_add_f32_e32 v4, 1.0, v4
	v_add_f32_e32 v2, 1.0, v2
	v_rcp_f32_e32 v4, v4
	v_rcp_f32_e32 v2, v2
	v_add_f32_e32 v3, 1.0, v3
	v_rcp_f32_e32 v3, v3
	v_exp_f32_e32 v5, v5
	v_fma_f32 v4, v4, -2.0, 1.0
	v_mul_f32_e32 v2, v2, v4
	v_add_f32_e32 v4, 1.0, v5
	v_fmac_f32_e32 v2, v177, v3
	v_rcp_f32_e32 v5, v4
	v_mul_f32_e32 v3, 0x4038aa3b, v2
	v_exp_f32_e32 v3, v3
	v_mov_b32_e32 v177, v2
	v_add_f32_e32 v3, 1.0, v3
	v_rcp_f32_e32 v3, v3
	s_nop 0
	v_fma_f32 v3, v3, -2.0, 1.0
	v_mul_f32_e32 v4, v5, v3
	v_fma_mixlo_f16 v3, v5, v3, 0
	v_and_b32_e32 v3, 0xffffbfff, v3
	v_or_b32_sdwa v108, s34, v3 dst_sel:DWORD dst_unused:UNUSED_PAD src0_sel:DWORD src1_sel:WORD_0
	s_nop 1
	v_mov_b32_dpp v109, v108 row_ror:8 row_mask:0xf bank_mask:0xf
	v_mov_b32_dpp v5, v4 row_ror:8 row_mask:0xf bank_mask:0xf
	s_and_saveexec_b64 s[12:13], s[0:1]
	v_lshl_or_b32 v108, v109, 16, v108
	s_andn2_b64 vcc, exec, s[4:5]
	s_cbranch_vccnz .Lpub_sc1
	buffer_store_dword v108, v176, s[8:11], 0 offen

.Lfirst_step:
	s_waitcnt vmcnt(0)
	v_cvt_pk_f16_f32 v180, v46, v47
	v_cvt_pk_f16_f32 v181, v48, v49
	v_cvt_pk_f16_f32 v182, v50, v51
	v_cvt_pk_f16_f32 v183, v52, v53
	v_cvt_pk_f16_f32 v218, v38, v39
	v_cvt_pk_f16_f32 v219, v40, v41
	v_cvt_pk_f16_f32 v220, v42, v43
	v_cvt_pk_f16_f32 v221, v44, v45
	s_branch .Lall_chunks_done
